# residual epilogues of P4/P7/P11: residual loads requested 3-6 row blocks ahead into spare VGPRs with counted vmcnt waits (were one round trip at a time)
# speedup vs baseline: 1.0059x; 1.0059x over previous
.LBB0_387:
	v_lshl_add_u32 v150, s24, 8, v152
	v_lshl_or_b32 v148, s26, 8, v154
	v_ashrrev_i32_e32 v151, 31, v150
	v_ashrrev_i32_e32 v149, 31, v148
	v_lshlrev_b64 v[160:161], 11, v[150:151]
	v_lshl_add_u64 v[168:169], v[160:161], 0, v[148:149]
	v_lshl_add_u64 v[170:171], v[168:169], 2, s[48:49]
	v_mov_b32_e32 v222, v170
	v_mov_b32_e32 v223, v171
	v_mov_b32_e32 v240, 0x20000
	v_mov_b32_e32 v241, 0
	global_load_dwordx4 v[174:177], v[222:223], off
	global_load_dwordx4 v[178:181], v[222:223], off offset:16
	global_load_dwordx4 v[182:185], v[222:223], off offset:512
	global_load_dwordx4 v[190:193], v[222:223], off offset:528
	v_lshl_add_u64 v[222:223], v[240:241], 0, v[222:223]
	global_load_dwordx4 v[194:197], v[222:223], off
	global_load_dwordx4 v[198:201], v[222:223], off offset:16
	global_load_dwordx4 v[202:205], v[222:223], off offset:512
	global_load_dwordx4 v[206:209], v[222:223], off offset:528
	v_lshl_add_u64 v[222:223], v[240:241], 0, v[222:223]
	global_load_dwordx4 v[210:213], v[222:223], off
	global_load_dwordx4 v[214:217], v[222:223], off offset:16
	global_load_dwordx4 v[218:221], v[222:223], off offset:512
	global_load_dwordx4 v[228:231], v[222:223], off offset:528
	s_nop 0
	s_nop 0
	v_lshl_add_u64 v[168:169], v[168:169], 1, s[50:51]
	s_waitcnt vmcnt(8)
	s_nop 1
	v_mov_b32_e32 v160, v174
	v_mov_b32_e32 v161, v175
	v_mov_b32_e32 v162, v176
	v_mov_b32_e32 v163, v177
	v_mov_b32_e32 v164, v178
	v_mov_b32_e32 v165, v179
	v_mov_b32_e32 v166, v180
	v_mov_b32_e32 v167, v181
	v_pk_add_f32 v[128:129], v[128:129], v[162:163]
	v_pk_add_f32 v[172:173], v[126:127], v[160:161]
	v_pk_add_f32 v[166:167], v[124:125], v[166:167]
	v_pk_add_f32 v[164:165], v[122:123], v[164:165]
	v_cvt_pk_bf16_f32 v122, v172, v173
	v_cvt_pk_bf16_f32 v123, v128, v129
	v_mul_f32_e32 v129, v129, v129
	v_cvt_pk_bf16_f32 v124, v164, v165
	v_cvt_pk_bf16_f32 v125, v166, v167
	global_store_dwordx4 v[168:169], v[122:125], off
	s_nop 0
	s_nop 0
	s_nop 0
	v_and_b32_e32 v123, 64, v159
	v_mul_f32_e32 v170, v173, v173
	v_mul_f32_e32 v165, v165, v165
	v_mul_f32_e32 v167, v167, v167
	v_xor_b32_e32 v122, 16, v159
	v_add_u32_e32 v123, 64, v123
	v_fmac_f32_e32 v170, v172, v172
	v_fmac_f32_e32 v129, v128, v128
	v_fmac_f32_e32 v165, v164, v164
	v_fmac_f32_e32 v167, v166, v166
	v_cmp_lt_i32_e32 vcc, v122, v123
	v_add_f32_e32 v128, v170, v129
	v_add_f32_e32 v129, v165, v167
	v_cndmask_b32_e32 v122, v159, v122, vcc
	v_add_f32_e32 v128, v128, v129
	v_lshlrev_b32_e32 v122, 2, v122
	s_nop 1
	v_mov_b32_e32 v124, v182
	v_mov_b32_e32 v125, v183
	v_mov_b32_e32 v126, v184
	v_mov_b32_e32 v127, v185
	v_pk_add_f32 v[120:121], v[120:121], v[126:127]
	v_pk_add_f32 v[118:119], v[118:119], v[124:125]
	s_nop 1
	v_mov_b32_e32 v160, v190
	v_mov_b32_e32 v161, v191
	v_mov_b32_e32 v162, v192
	v_mov_b32_e32 v163, v193
	v_lshl_add_u64 v[222:223], v[240:241], 0, v[222:223]
	global_load_dwordx4 v[174:177], v[222:223], off
	global_load_dwordx4 v[178:181], v[222:223], off offset:16
	global_load_dwordx4 v[182:185], v[222:223], off offset:512
	global_load_dwordx4 v[190:193], v[222:223], off offset:528
	v_pk_add_f32 v[124:125], v[116:117], v[162:163]
	v_pk_add_f32 v[126:127], v[114:115], v[160:161]
	v_mul_f32_e32 v114, v119, v119
	v_mul_f32_e32 v115, v121, v121
	v_mul_f32_e32 v116, v127, v127
	v_mul_f32_e32 v117, v125, v125
	v_fmac_f32_e32 v114, v118, v118
	v_fmac_f32_e32 v115, v120, v120
	v_fmac_f32_e32 v116, v126, v126
	v_fmac_f32_e32 v117, v124, v124
	v_add_f32_e32 v114, v114, v115
	v_add_f32_e32 v115, v116, v117
	v_add_f32_e32 v114, v114, v115
	v_add_f32_e32 v114, v128, v114
	ds_bpermute_b32 v115, v122, v114
	v_xor_b32_e32 v116, 32, v159
	v_cmp_lt_i32_e32 vcc, v116, v123
	v_cvt_pk_bf16_f32 v118, v118, v119
	v_cvt_pk_bf16_f32 v119, v120, v121
	s_waitcnt lgkmcnt(0)
	v_add_f32_e32 v114, v114, v115
	v_cvt_pk_bf16_f32 v120, v126, v127
	v_cvt_pk_bf16_f32 v121, v124, v125
	v_cndmask_b32_e32 v116, v159, v116, vcc
	v_lshlrev_b32_e32 v116, 2, v116
	ds_bpermute_b32 v115, v116, v114
	global_store_dwordx4 v[168:169], v[118:121], off offset:256
	s_and_saveexec_b64 s[24:25], s[4:5]
	s_cbranch_execz .LBB0_389
	s_waitcnt lgkmcnt(0)
	v_add_f32_e32 v114, v114, v115
	v_fma_f32 v114, v114, s55, 0.5
	v_trunc_f32_e32 v114, v114
	v_mul_f32_e32 v115, 0x2f800000, v114
	v_floor_f32_e32 v115, v115
	v_fmac_f32_e32 v114, 0xcf800000, v115
	v_cvt_u32_f32_e32 v114, v114
	v_cvt_u32_f32_e32 v115, v115
	v_lshl_add_u64 v[118:119], v[150:151], 3, s[10:11]
	global_atomic_add_x2 v[118:119], v[114:115], off
.LBB0_389:
	s_or_b64 exec, exec, s[24:25]
	v_or_b32_e32 v114, 16, v150
	s_waitcnt lgkmcnt(0)
	v_ashrrev_i32_e32 v115, 31, v114
	v_lshlrev_b64 v[118:119], 11, v[114:115]
	v_lshl_add_u64 v[128:129], v[118:119], 0, v[148:149]
	v_lshl_add_u64 v[160:161], v[128:129], 2, s[48:49]
	s_nop 0
	s_nop 0
	v_lshl_add_u64 v[128:129], v[128:129], 1, s[50:51]
	s_waitcnt vmcnt(10)
	s_nop 1
	v_mov_b32_e32 v118, v194
	v_mov_b32_e32 v119, v195
	v_mov_b32_e32 v120, v196
	v_mov_b32_e32 v121, v197
	v_pk_add_f32 v[120:121], v[112:113], v[120:121]
	v_pk_add_f32 v[118:119], v[110:111], v[118:119]
	s_nop 1
	v_mov_b32_e32 v124, v198
	v_mov_b32_e32 v125, v199
	v_mov_b32_e32 v126, v200
	v_mov_b32_e32 v127, v201
	v_pk_add_f32 v[126:127], v[108:109], v[126:127]
	v_pk_add_f32 v[124:125], v[106:107], v[124:125]
	v_cvt_pk_bf16_f32 v106, v118, v119
	v_cvt_pk_bf16_f32 v107, v120, v121
	v_mul_f32_e32 v117, v119, v119
	v_cvt_pk_bf16_f32 v108, v124, v125
	v_cvt_pk_bf16_f32 v109, v126, v127
	global_store_dwordx4 v[128:129], v[106:109], off
	s_nop 0
	s_nop 0
	s_nop 0
	v_mul_f32_e32 v119, v121, v121
	v_mul_f32_e32 v121, v125, v125
	v_mul_f32_e32 v123, v127, v127
	v_fmac_f32_e32 v117, v118, v118
	v_fmac_f32_e32 v119, v120, v120
	v_fmac_f32_e32 v121, v124, v124
	v_fmac_f32_e32 v123, v126, v126
	v_add_f32_e32 v117, v117, v119
	v_add_f32_e32 v118, v121, v123
	v_add_f32_e32 v117, v117, v118
	s_nop 1
	v_mov_b32_e32 v106, v202
	v_mov_b32_e32 v107, v203
	v_mov_b32_e32 v108, v204
	v_mov_b32_e32 v109, v205
	v_pk_add_f32 v[104:105], v[104:105], v[108:109]
	v_pk_add_f32 v[102:103], v[102:103], v[106:107]
	s_nop 1
	v_mov_b32_e32 v110, v206
	v_mov_b32_e32 v111, v207
	v_mov_b32_e32 v112, v208
	v_mov_b32_e32 v113, v209
	v_lshl_add_u64 v[222:223], v[240:241], 2, v[222:223]
	v_lshl_add_u64 v[222:223], v[240:241], 0, v[222:223]
	global_load_dwordx4 v[194:197], v[222:223], off
	global_load_dwordx4 v[198:201], v[222:223], off offset:16
	global_load_dwordx4 v[202:205], v[222:223], off offset:512
	global_load_dwordx4 v[206:209], v[222:223], off offset:528
	v_pk_add_f32 v[106:107], v[100:101], v[112:113]
	v_pk_add_f32 v[108:109], v[98:99], v[110:111]
	v_mul_f32_e32 v98, v103, v103
	v_mul_f32_e32 v99, v105, v105
	v_mul_f32_e32 v100, v109, v109
	v_mul_f32_e32 v101, v107, v107
	v_fmac_f32_e32 v98, v102, v102
	v_fmac_f32_e32 v99, v104, v104
	v_fmac_f32_e32 v100, v108, v108
	v_fmac_f32_e32 v101, v106, v106
	v_add_f32_e32 v98, v98, v99
	v_add_f32_e32 v99, v100, v101
	v_add_f32_e32 v98, v98, v99
	v_add_f32_e32 v98, v117, v98
	ds_bpermute_b32 v99, v122, v98
	v_cvt_pk_bf16_f32 v100, v102, v103
	v_cvt_pk_bf16_f32 v101, v104, v105
	v_cvt_pk_bf16_f32 v102, v108, v109
	v_cvt_pk_bf16_f32 v103, v106, v107
	s_waitcnt lgkmcnt(0)
	v_add_f32_e32 v98, v98, v99
	ds_bpermute_b32 v99, v116, v98
	global_store_dwordx4 v[128:129], v[100:103], off offset:256
	s_and_saveexec_b64 s[24:25], s[4:5]
	s_cbranch_execz .LBB0_391
	s_waitcnt lgkmcnt(0)
	v_add_f32_e32 v98, v98, v99
	v_fma_f32 v98, v98, s55, 0.5
	v_trunc_f32_e32 v98, v98
	v_mul_f32_e32 v99, 0x2f800000, v98
	v_floor_f32_e32 v99, v99
	v_fmac_f32_e32 v98, 0xcf800000, v99
	v_cvt_u32_f32_e32 v98, v98
	v_cvt_u32_f32_e32 v99, v99
	v_lshl_add_u64 v[100:101], v[114:115], 3, s[10:11]
	global_atomic_add_x2 v[100:101], v[98:99], off
.LBB0_391:
	s_or_b64 exec, exec, s[24:25]
	v_or_b32_e32 v98, 32, v150
	s_waitcnt lgkmcnt(0)
	v_ashrrev_i32_e32 v99, 31, v98
	v_lshlrev_b64 v[100:101], 11, v[98:99]
	v_lshl_add_u64 v[108:109], v[100:101], 0, v[148:149]
	v_lshl_add_u64 v[110:111], v[108:109], 2, s[48:49]
	s_nop 0
	s_nop 0
	v_lshl_add_u64 v[108:109], v[108:109], 1, s[50:51]
	s_waitcnt vmcnt(12)
	s_nop 1
	v_mov_b32_e32 v100, v210
	v_mov_b32_e32 v101, v211
	v_mov_b32_e32 v102, v212
	v_mov_b32_e32 v103, v213
	v_pk_add_f32 v[102:103], v[96:97], v[102:103]
	v_pk_add_f32 v[100:101], v[94:95], v[100:101]
	s_nop 1
	v_mov_b32_e32 v104, v214
	v_mov_b32_e32 v105, v215
	v_mov_b32_e32 v106, v216
	v_mov_b32_e32 v107, v217
	v_pk_add_f32 v[106:107], v[92:93], v[106:107]
	v_pk_add_f32 v[104:105], v[90:91], v[104:105]
	v_cvt_pk_bf16_f32 v90, v100, v101
	v_cvt_pk_bf16_f32 v91, v102, v103
	v_mul_f32_e32 v101, v101, v101
	v_cvt_pk_bf16_f32 v92, v104, v105
	v_cvt_pk_bf16_f32 v93, v106, v107
	global_store_dwordx4 v[108:109], v[90:93], off
	s_nop 0
	s_nop 0
	s_nop 0
	v_mul_f32_e32 v103, v103, v103
	v_mul_f32_e32 v105, v105, v105
	v_mul_f32_e32 v107, v107, v107
	v_fmac_f32_e32 v101, v100, v100
	v_fmac_f32_e32 v103, v102, v102
	v_fmac_f32_e32 v105, v104, v104
	v_fmac_f32_e32 v107, v106, v106
	v_add_f32_e32 v100, v101, v103
	v_add_f32_e32 v101, v105, v107
	v_add_f32_e32 v100, v100, v101
	s_nop 1
	v_mov_b32_e32 v90, v218
	v_mov_b32_e32 v91, v219
	v_mov_b32_e32 v92, v220
	v_mov_b32_e32 v93, v221
	v_pk_add_f32 v[88:89], v[88:89], v[92:93]
	v_pk_add_f32 v[86:87], v[86:87], v[90:91]
	s_nop 1
	v_mov_b32_e32 v94, v228
	v_mov_b32_e32 v95, v229
	v_mov_b32_e32 v96, v230
	v_mov_b32_e32 v97, v231
	v_lshl_add_u64 v[222:223], v[240:241], 0, v[222:223]
	global_load_dwordx4 v[210:213], v[222:223], off
	global_load_dwordx4 v[214:217], v[222:223], off offset:16
	global_load_dwordx4 v[218:221], v[222:223], off offset:512
	global_load_dwordx4 v[228:231], v[222:223], off offset:528
	v_pk_add_f32 v[90:91], v[84:85], v[96:97]
	v_pk_add_f32 v[92:93], v[82:83], v[94:95]
	v_mul_f32_e32 v82, v87, v87
	v_mul_f32_e32 v83, v89, v89
	v_mul_f32_e32 v84, v93, v93
	v_mul_f32_e32 v85, v91, v91
	v_fmac_f32_e32 v82, v86, v86
	v_fmac_f32_e32 v83, v88, v88
	v_fmac_f32_e32 v84, v92, v92
	v_fmac_f32_e32 v85, v90, v90
	v_add_f32_e32 v82, v82, v83
	v_add_f32_e32 v83, v84, v85
	v_add_f32_e32 v82, v82, v83
	v_add_f32_e32 v82, v100, v82
	ds_bpermute_b32 v83, v122, v82
	v_cvt_pk_bf16_f32 v84, v86, v87
	v_cvt_pk_bf16_f32 v85, v88, v89
	v_cvt_pk_bf16_f32 v86, v92, v93
	v_cvt_pk_bf16_f32 v87, v90, v91
	s_waitcnt lgkmcnt(0)
	v_add_f32_e32 v82, v82, v83
	ds_bpermute_b32 v83, v116, v82
	global_store_dwordx4 v[108:109], v[84:87], off offset:256
	s_and_saveexec_b64 s[24:25], s[4:5]
	s_cbranch_execz .LBB0_393
	s_waitcnt lgkmcnt(0)
	v_add_f32_e32 v82, v82, v83
	v_fma_f32 v82, v82, s55, 0.5
	v_trunc_f32_e32 v82, v82
	v_mul_f32_e32 v83, 0x2f800000, v82
	v_floor_f32_e32 v83, v83
	v_fmac_f32_e32 v82, 0xcf800000, v83
	v_cvt_u32_f32_e32 v82, v82
	v_cvt_u32_f32_e32 v83, v83
	v_lshl_add_u64 v[84:85], v[98:99], 3, s[10:11]
	global_atomic_add_x2 v[84:85], v[82:83], off
.LBB0_393:
	s_or_b64 exec, exec, s[24:25]
	v_or_b32_e32 v82, 48, v150
	s_waitcnt lgkmcnt(0)
	v_ashrrev_i32_e32 v83, 31, v82
	v_lshlrev_b64 v[84:85], 11, v[82:83]
	v_lshl_add_u64 v[92:93], v[84:85], 0, v[148:149]
	v_lshl_add_u64 v[94:95], v[92:93], 2, s[48:49]
	s_nop 0
	s_nop 0
	v_lshl_add_u64 v[92:93], v[92:93], 1, s[50:51]
	s_waitcnt vmcnt(13)
	s_nop 1
	v_mov_b32_e32 v84, v174
	v_mov_b32_e32 v85, v175
	v_mov_b32_e32 v86, v176
	v_mov_b32_e32 v87, v177
	v_pk_add_f32 v[86:87], v[80:81], v[86:87]
	v_pk_add_f32 v[84:85], v[78:79], v[84:85]
	s_nop 1
	v_mov_b32_e32 v88, v178
	v_mov_b32_e32 v89, v179
	v_mov_b32_e32 v90, v180
	v_mov_b32_e32 v91, v181
	v_pk_add_f32 v[90:91], v[76:77], v[90:91]
	v_pk_add_f32 v[88:89], v[74:75], v[88:89]
	v_cvt_pk_bf16_f32 v74, v84, v85
	v_cvt_pk_bf16_f32 v75, v86, v87
	v_mul_f32_e32 v85, v85, v85
	v_cvt_pk_bf16_f32 v76, v88, v89
	v_cvt_pk_bf16_f32 v77, v90, v91
	global_store_dwordx4 v[92:93], v[74:77], off
	s_nop 0
	s_nop 0
	s_nop 0
	v_mul_f32_e32 v87, v87, v87
	v_mul_f32_e32 v89, v89, v89
	v_mul_f32_e32 v91, v91, v91
	v_fmac_f32_e32 v85, v84, v84
	v_fmac_f32_e32 v87, v86, v86
	v_fmac_f32_e32 v89, v88, v88
	v_fmac_f32_e32 v91, v90, v90
	v_add_f32_e32 v84, v85, v87
	v_add_f32_e32 v85, v89, v91
	v_add_f32_e32 v84, v84, v85
	s_nop 1
	v_mov_b32_e32 v74, v182
	v_mov_b32_e32 v75, v183
	v_mov_b32_e32 v76, v184
	v_mov_b32_e32 v77, v185
	v_pk_add_f32 v[72:73], v[72:73], v[76:77]
	v_pk_add_f32 v[70:71], v[70:71], v[74:75]
	s_nop 1
	v_mov_b32_e32 v78, v190
	v_mov_b32_e32 v79, v191
	v_mov_b32_e32 v80, v192
	v_mov_b32_e32 v81, v193
	v_lshl_add_u64 v[222:223], v[240:241], 0, v[222:223]
	global_load_dwordx4 v[174:177], v[222:223], off
	global_load_dwordx4 v[178:181], v[222:223], off offset:16
	global_load_dwordx4 v[182:185], v[222:223], off offset:512
	global_load_dwordx4 v[190:193], v[222:223], off offset:528
	v_pk_add_f32 v[74:75], v[68:69], v[80:81]
	v_pk_add_f32 v[76:77], v[66:67], v[78:79]
	v_mul_f32_e32 v66, v71, v71
	v_mul_f32_e32 v67, v73, v73
	v_mul_f32_e32 v68, v77, v77
	v_mul_f32_e32 v69, v75, v75
	v_fmac_f32_e32 v66, v70, v70
	v_fmac_f32_e32 v67, v72, v72
	v_fmac_f32_e32 v68, v76, v76
	v_fmac_f32_e32 v69, v74, v74
	v_add_f32_e32 v66, v66, v67
	v_add_f32_e32 v67, v68, v69
	v_add_f32_e32 v66, v66, v67
	v_add_f32_e32 v66, v84, v66
	ds_bpermute_b32 v67, v122, v66
	v_cvt_pk_bf16_f32 v68, v70, v71
	v_cvt_pk_bf16_f32 v69, v72, v73
	v_cvt_pk_bf16_f32 v70, v76, v77
	v_cvt_pk_bf16_f32 v71, v74, v75
	s_waitcnt lgkmcnt(0)
	v_add_f32_e32 v66, v66, v67
	ds_bpermute_b32 v67, v116, v66
	global_store_dwordx4 v[92:93], v[68:71], off offset:256
	s_and_saveexec_b64 s[24:25], s[4:5]
	s_cbranch_execz .LBB0_395
	s_waitcnt lgkmcnt(0)
	v_add_f32_e32 v66, v66, v67
	v_fma_f32 v66, v66, s55, 0.5
	v_trunc_f32_e32 v66, v66
	v_mul_f32_e32 v67, 0x2f800000, v66
	v_floor_f32_e32 v67, v67
	v_fmac_f32_e32 v66, 0xcf800000, v67
	v_cvt_u32_f32_e32 v66, v66
	v_cvt_u32_f32_e32 v67, v67
	v_lshl_add_u64 v[68:69], v[82:83], 3, s[10:11]
	global_atomic_add_x2 v[68:69], v[66:67], off
.LBB0_395:
	s_or_b64 exec, exec, s[24:25]
	v_add_u32_e32 v66, 0x80, v150
	s_waitcnt lgkmcnt(0)
	v_ashrrev_i32_e32 v67, 31, v66
	v_lshlrev_b64 v[68:69], 11, v[66:67]
	v_lshl_add_u64 v[76:77], v[68:69], 0, v[148:149]
	v_lshl_add_u64 v[78:79], v[76:77], 2, s[48:49]
	s_nop 0
	s_nop 0
	v_lshl_add_u64 v[76:77], v[76:77], 1, s[50:51]
	s_waitcnt vmcnt(13)
	s_nop 1
	v_mov_b32_e32 v68, v194
	v_mov_b32_e32 v69, v195
	v_mov_b32_e32 v70, v196
	v_mov_b32_e32 v71, v197
	v_pk_add_f32 v[70:71], v[64:65], v[70:71]
	v_pk_add_f32 v[68:69], v[62:63], v[68:69]
	s_nop 1
	v_mov_b32_e32 v72, v198
	v_mov_b32_e32 v73, v199
	v_mov_b32_e32 v74, v200
	v_mov_b32_e32 v75, v201
	v_pk_add_f32 v[74:75], v[60:61], v[74:75]
	v_pk_add_f32 v[72:73], v[58:59], v[72:73]
	v_cvt_pk_bf16_f32 v58, v68, v69
	v_cvt_pk_bf16_f32 v59, v70, v71
	v_mul_f32_e32 v69, v69, v69
	v_cvt_pk_bf16_f32 v60, v72, v73
	v_cvt_pk_bf16_f32 v61, v74, v75
	global_store_dwordx4 v[76:77], v[58:61], off
	s_nop 0
	s_nop 0
	s_nop 0
	v_mul_f32_e32 v71, v71, v71
	v_mul_f32_e32 v73, v73, v73
	v_mul_f32_e32 v75, v75, v75
	v_fmac_f32_e32 v69, v68, v68
	v_fmac_f32_e32 v71, v70, v70
	v_fmac_f32_e32 v73, v72, v72
	v_fmac_f32_e32 v75, v74, v74
	v_add_f32_e32 v68, v69, v71
	v_add_f32_e32 v69, v73, v75
	v_add_f32_e32 v68, v68, v69
	s_nop 1
	v_mov_b32_e32 v58, v202
	v_mov_b32_e32 v59, v203
	v_mov_b32_e32 v60, v204
	v_mov_b32_e32 v61, v205
	v_pk_add_f32 v[56:57], v[56:57], v[60:61]
	v_pk_add_f32 v[54:55], v[54:55], v[58:59]
	s_nop 1
	v_mov_b32_e32 v62, v206
	v_mov_b32_e32 v63, v207
	v_mov_b32_e32 v64, v208
	v_mov_b32_e32 v65, v209
	v_lshl_add_u64 v[222:223], v[240:241], 0, v[222:223]
	global_load_dwordx4 v[194:197], v[222:223], off
	global_load_dwordx4 v[198:201], v[222:223], off offset:16
	global_load_dwordx4 v[202:205], v[222:223], off offset:512
	global_load_dwordx4 v[206:209], v[222:223], off offset:528
	v_pk_add_f32 v[58:59], v[52:53], v[64:65]
	v_pk_add_f32 v[60:61], v[50:51], v[62:63]
	v_mul_f32_e32 v50, v55, v55
	v_mul_f32_e32 v51, v57, v57
	v_mul_f32_e32 v52, v61, v61
	v_mul_f32_e32 v53, v59, v59
	v_fmac_f32_e32 v50, v54, v54
	v_fmac_f32_e32 v51, v56, v56
	v_fmac_f32_e32 v52, v60, v60
	v_fmac_f32_e32 v53, v58, v58
	v_add_f32_e32 v50, v50, v51
	v_add_f32_e32 v51, v52, v53
	v_add_f32_e32 v50, v50, v51
	v_add_f32_e32 v50, v68, v50
	ds_bpermute_b32 v51, v122, v50
	v_cvt_pk_bf16_f32 v52, v54, v55
	v_cvt_pk_bf16_f32 v53, v56, v57
	v_cvt_pk_bf16_f32 v54, v60, v61
	v_cvt_pk_bf16_f32 v55, v58, v59
	s_waitcnt lgkmcnt(0)
	v_add_f32_e32 v50, v50, v51
	ds_bpermute_b32 v51, v116, v50
	global_store_dwordx4 v[76:77], v[52:55], off offset:256
	s_and_saveexec_b64 s[24:25], s[4:5]
	s_cbranch_execz .LBB0_397
	s_waitcnt lgkmcnt(0)
	v_add_f32_e32 v50, v50, v51
	v_fma_f32 v50, v50, s55, 0.5
	v_trunc_f32_e32 v50, v50
	v_mul_f32_e32 v51, 0x2f800000, v50
	v_floor_f32_e32 v51, v51
	v_fmac_f32_e32 v50, 0xcf800000, v51
	v_cvt_u32_f32_e32 v50, v50
	v_cvt_u32_f32_e32 v51, v51
	v_lshl_add_u64 v[52:53], v[66:67], 3, s[10:11]
	global_atomic_add_x2 v[52:53], v[50:51], off
.LBB0_397:
	s_or_b64 exec, exec, s[24:25]
	v_add_u32_e32 v50, 0x90, v150
	s_waitcnt lgkmcnt(0)
	v_ashrrev_i32_e32 v51, 31, v50
	v_lshlrev_b64 v[52:53], 11, v[50:51]
	v_lshl_add_u64 v[60:61], v[52:53], 0, v[148:149]
	v_lshl_add_u64 v[62:63], v[60:61], 2, s[48:49]
	s_nop 0
	s_nop 0
	v_lshl_add_u64 v[60:61], v[60:61], 1, s[50:51]
	s_waitcnt vmcnt(13)
	s_nop 1
	v_mov_b32_e32 v52, v210
	v_mov_b32_e32 v53, v211
	v_mov_b32_e32 v54, v212
	v_mov_b32_e32 v55, v213
	v_pk_add_f32 v[54:55], v[48:49], v[54:55]
	v_pk_add_f32 v[52:53], v[46:47], v[52:53]
	s_nop 1
	v_mov_b32_e32 v56, v214
	v_mov_b32_e32 v57, v215
	v_mov_b32_e32 v58, v216
	v_mov_b32_e32 v59, v217
	v_pk_add_f32 v[58:59], v[44:45], v[58:59]
	v_pk_add_f32 v[56:57], v[42:43], v[56:57]
	v_cvt_pk_bf16_f32 v42, v52, v53
	v_cvt_pk_bf16_f32 v43, v54, v55
	v_mul_f32_e32 v53, v53, v53
	v_cvt_pk_bf16_f32 v44, v56, v57
	v_cvt_pk_bf16_f32 v45, v58, v59
	global_store_dwordx4 v[60:61], v[42:45], off
	s_nop 0
	s_nop 0
	s_nop 0
	v_mul_f32_e32 v55, v55, v55
	v_mul_f32_e32 v57, v57, v57
	v_mul_f32_e32 v59, v59, v59
	v_fmac_f32_e32 v53, v52, v52
	v_fmac_f32_e32 v55, v54, v54
	v_fmac_f32_e32 v57, v56, v56
	v_fmac_f32_e32 v59, v58, v58
	v_add_f32_e32 v52, v53, v55
	v_add_f32_e32 v53, v57, v59
	v_add_f32_e32 v52, v52, v53
	s_nop 1
	v_mov_b32_e32 v42, v218
	v_mov_b32_e32 v43, v219
	v_mov_b32_e32 v44, v220
	v_mov_b32_e32 v45, v221
	v_pk_add_f32 v[40:41], v[40:41], v[44:45]
	v_pk_add_f32 v[38:39], v[38:39], v[42:43]
	s_nop 1
	v_mov_b32_e32 v46, v228
	v_mov_b32_e32 v47, v229
	v_mov_b32_e32 v48, v230
	v_mov_b32_e32 v49, v231
	v_pk_add_f32 v[42:43], v[36:37], v[48:49]
	v_pk_add_f32 v[44:45], v[34:35], v[46:47]
	v_mul_f32_e32 v34, v39, v39
	v_mul_f32_e32 v35, v41, v41
	v_mul_f32_e32 v36, v45, v45
	v_mul_f32_e32 v37, v43, v43
	v_fmac_f32_e32 v34, v38, v38
	v_fmac_f32_e32 v35, v40, v40
	v_fmac_f32_e32 v36, v44, v44
	v_fmac_f32_e32 v37, v42, v42
	v_add_f32_e32 v34, v34, v35
	v_add_f32_e32 v35, v36, v37
	v_add_f32_e32 v34, v34, v35
	v_add_f32_e32 v34, v52, v34
	ds_bpermute_b32 v35, v122, v34
	v_cvt_pk_bf16_f32 v36, v38, v39
	v_cvt_pk_bf16_f32 v37, v40, v41
	v_cvt_pk_bf16_f32 v38, v44, v45
	v_cvt_pk_bf16_f32 v39, v42, v43
	s_waitcnt lgkmcnt(0)
	v_add_f32_e32 v34, v34, v35
	ds_bpermute_b32 v35, v116, v34
	global_store_dwordx4 v[60:61], v[36:39], off offset:256
	s_and_saveexec_b64 s[24:25], s[4:5]
	s_cbranch_execz .LBB0_399
	s_waitcnt lgkmcnt(0)
	v_add_f32_e32 v34, v34, v35
	v_fma_f32 v34, v34, s55, 0.5
	v_trunc_f32_e32 v34, v34
	v_mul_f32_e32 v35, 0x2f800000, v34
	v_floor_f32_e32 v35, v35
	v_fmac_f32_e32 v34, 0xcf800000, v35
	v_cvt_u32_f32_e32 v34, v34
	v_cvt_u32_f32_e32 v35, v35
	v_lshl_add_u64 v[36:37], v[50:51], 3, s[10:11]
	global_atomic_add_x2 v[36:37], v[34:35], off
.LBB0_399:
	s_or_b64 exec, exec, s[24:25]
	v_add_u32_e32 v34, 0xa0, v150
	s_waitcnt lgkmcnt(0)
	v_ashrrev_i32_e32 v35, 31, v34
	v_lshlrev_b64 v[36:37], 11, v[34:35]
	v_lshl_add_u64 v[44:45], v[36:37], 0, v[148:149]
	v_lshl_add_u64 v[46:47], v[44:45], 2, s[48:49]
	s_nop 0
	s_nop 0
	v_lshl_add_u64 v[44:45], v[44:45], 1, s[50:51]
	s_waitcnt vmcnt(9)
	s_nop 1
	v_mov_b32_e32 v36, v174
	v_mov_b32_e32 v37, v175
	v_mov_b32_e32 v38, v176
	v_mov_b32_e32 v39, v177
	v_pk_add_f32 v[38:39], v[32:33], v[38:39]
	v_pk_add_f32 v[36:37], v[30:31], v[36:37]
	s_nop 1
	v_mov_b32_e32 v40, v178
	v_mov_b32_e32 v41, v179
	v_mov_b32_e32 v42, v180
	v_mov_b32_e32 v43, v181
	v_pk_add_f32 v[42:43], v[28:29], v[42:43]
	v_pk_add_f32 v[40:41], v[26:27], v[40:41]
	v_cvt_pk_bf16_f32 v26, v36, v37
	v_cvt_pk_bf16_f32 v27, v38, v39
	v_mul_f32_e32 v37, v37, v37
	v_cvt_pk_bf16_f32 v28, v40, v41
	v_cvt_pk_bf16_f32 v29, v42, v43
	global_store_dwordx4 v[44:45], v[26:29], off
	s_nop 0
	s_nop 0
	s_nop 0
	v_mul_f32_e32 v39, v39, v39
	v_mul_f32_e32 v41, v41, v41
	v_mul_f32_e32 v43, v43, v43
	v_fmac_f32_e32 v37, v36, v36
	v_fmac_f32_e32 v39, v38, v38
	v_fmac_f32_e32 v41, v40, v40
	v_fmac_f32_e32 v43, v42, v42
	v_add_f32_e32 v36, v37, v39
	v_add_f32_e32 v37, v41, v43
	v_add_f32_e32 v36, v36, v37
	s_nop 1
	v_mov_b32_e32 v26, v182
	v_mov_b32_e32 v27, v183
	v_mov_b32_e32 v28, v184
	v_mov_b32_e32 v29, v185
	v_pk_add_f32 v[24:25], v[24:25], v[28:29]
	v_pk_add_f32 v[22:23], v[22:23], v[26:27]
	s_nop 1
	v_mov_b32_e32 v30, v190
	v_mov_b32_e32 v31, v191
	v_mov_b32_e32 v32, v192
	v_mov_b32_e32 v33, v193
	v_pk_add_f32 v[26:27], v[20:21], v[32:33]
	v_pk_add_f32 v[28:29], v[18:19], v[30:31]
	v_mul_f32_e32 v18, v23, v23
	v_mul_f32_e32 v19, v25, v25
	v_mul_f32_e32 v20, v29, v29
	v_mul_f32_e32 v21, v27, v27
	v_fmac_f32_e32 v18, v22, v22
	v_fmac_f32_e32 v19, v24, v24
	v_fmac_f32_e32 v20, v28, v28
	v_fmac_f32_e32 v21, v26, v26
	v_add_f32_e32 v18, v18, v19
	v_add_f32_e32 v19, v20, v21
	v_add_f32_e32 v18, v18, v19
	v_add_f32_e32 v18, v36, v18
	ds_bpermute_b32 v19, v122, v18
	v_cvt_pk_bf16_f32 v20, v22, v23
	v_cvt_pk_bf16_f32 v21, v24, v25
	v_cvt_pk_bf16_f32 v22, v28, v29
	v_cvt_pk_bf16_f32 v23, v26, v27
	s_waitcnt lgkmcnt(0)
	v_add_f32_e32 v18, v18, v19
	ds_bpermute_b32 v19, v116, v18
	global_store_dwordx4 v[44:45], v[20:23], off offset:256
	s_and_saveexec_b64 s[24:25], s[4:5]
	s_cbranch_execz .LBB0_401
	s_waitcnt lgkmcnt(0)
	v_add_f32_e32 v18, v18, v19
	v_fma_f32 v18, v18, s55, 0.5
	v_trunc_f32_e32 v18, v18
	v_mul_f32_e32 v19, 0x2f800000, v18
	v_floor_f32_e32 v19, v19
	v_fmac_f32_e32 v18, 0xcf800000, v19
	v_cvt_u32_f32_e32 v18, v18
	v_cvt_u32_f32_e32 v19, v19
	v_lshl_add_u64 v[20:21], v[34:35], 3, s[10:11]
	global_atomic_add_x2 v[20:21], v[18:19], off
.LBB0_401:
	s_or_b64 exec, exec, s[24:25]
	v_add_u32_e32 v18, 0xb0, v150
	s_waitcnt lgkmcnt(0)
	v_ashrrev_i32_e32 v19, 31, v18
	v_lshlrev_b64 v[20:21], 11, v[18:19]
	v_lshl_add_u64 v[28:29], v[20:21], 0, v[148:149]
	v_lshl_add_u64 v[30:31], v[28:29], 2, s[48:49]
	s_nop 0
	s_nop 0
	v_lshl_add_u64 v[28:29], v[28:29], 1, s[50:51]
	s_waitcnt vmcnt(5)
	s_nop 1
	v_mov_b32_e32 v20, v194
	v_mov_b32_e32 v21, v195
	v_mov_b32_e32 v22, v196
	v_mov_b32_e32 v23, v197
	v_pk_add_f32 v[22:23], v[16:17], v[22:23]
	v_pk_add_f32 v[20:21], v[14:15], v[20:21]
	s_nop 1
	v_mov_b32_e32 v24, v198
	v_mov_b32_e32 v25, v199
	v_mov_b32_e32 v26, v200
	v_mov_b32_e32 v27, v201
	v_pk_add_f32 v[26:27], v[12:13], v[26:27]
	v_pk_add_f32 v[24:25], v[10:11], v[24:25]
	v_cvt_pk_bf16_f32 v10, v20, v21
	v_cvt_pk_bf16_f32 v11, v22, v23
	v_mul_f32_e32 v21, v21, v21
	v_cvt_pk_bf16_f32 v12, v24, v25
	v_cvt_pk_bf16_f32 v13, v26, v27
	global_store_dwordx4 v[28:29], v[10:13], off
	s_nop 0
	s_nop 0
	s_nop 0
	v_mul_f32_e32 v23, v23, v23
	v_mul_f32_e32 v25, v25, v25
	v_mul_f32_e32 v27, v27, v27
	v_fmac_f32_e32 v21, v20, v20
	v_fmac_f32_e32 v23, v22, v22
	v_fmac_f32_e32 v25, v24, v24
	v_fmac_f32_e32 v27, v26, v26
	v_add_f32_e32 v20, v21, v23
	v_add_f32_e32 v21, v25, v27
	v_add_f32_e32 v20, v20, v21
	s_nop 1
	v_mov_b32_e32 v10, v202
	v_mov_b32_e32 v11, v203
	v_mov_b32_e32 v12, v204
	v_mov_b32_e32 v13, v205
	v_pk_add_f32 v[8:9], v[8:9], v[12:13]
	v_pk_add_f32 v[6:7], v[6:7], v[10:11]
	s_nop 1
	v_mov_b32_e32 v14, v206
	v_mov_b32_e32 v15, v207
	v_mov_b32_e32 v16, v208
	v_mov_b32_e32 v17, v209
	v_pk_add_f32 v[10:11], v[4:5], v[16:17]
	v_pk_add_f32 v[12:13], v[2:3], v[14:15]
	v_mul_f32_e32 v2, v7, v7
	v_mul_f32_e32 v3, v9, v9
	v_mul_f32_e32 v4, v13, v13
	v_mul_f32_e32 v5, v11, v11
	v_fmac_f32_e32 v2, v6, v6
	v_fmac_f32_e32 v3, v8, v8
	v_fmac_f32_e32 v4, v12, v12
	v_fmac_f32_e32 v5, v10, v10
	v_add_f32_e32 v2, v2, v3
	v_add_f32_e32 v3, v4, v5
	v_add_f32_e32 v2, v2, v3
	v_add_f32_e32 v2, v20, v2
	ds_bpermute_b32 v3, v122, v2
	v_cvt_pk_bf16_f32 v4, v6, v7
	v_cvt_pk_bf16_f32 v5, v8, v9
	v_cvt_pk_bf16_f32 v6, v12, v13
	v_cvt_pk_bf16_f32 v7, v10, v11
	s_waitcnt lgkmcnt(0)
	v_add_f32_e32 v2, v2, v3
	ds_bpermute_b32 v3, v116, v2
	global_store_dwordx4 v[28:29], v[4:7], off offset:256
	s_and_saveexec_b64 s[24:25], s[4:5]
	s_cbranch_execz .LBB0_403
	s_waitcnt lgkmcnt(0)
	v_add_f32_e32 v2, v2, v3
	v_fma_f32 v2, v2, s55, 0.5
	v_trunc_f32_e32 v2, v2
	v_mul_f32_e32 v3, 0x2f800000, v2
	v_floor_f32_e32 v3, v3
	v_fmac_f32_e32 v2, 0xcf800000, v3
	v_cvt_u32_f32_e32 v2, v2
	v_cvt_u32_f32_e32 v3, v3
	v_lshl_add_u64 v[4:5], v[18:19], 3, s[10:11]
	global_atomic_add_x2 v[4:5], v[2:3], off

.LBB0_559:
	v_lshl_add_u32 v150, s45, 8, v152
	v_ashrrev_i32_e32 v151, 31, v150
	v_lshl_or_b32 v148, s48, 8, v154
	v_lshlrev_b64 v[162:163], 12, v[150:151]
	v_ashrrev_i32_e32 v149, 31, v148
	v_lshl_add_u64 v[162:163], s[50:51], 0, v[162:163]
	v_lshl_add_u64 v[166:167], v[148:149], 1, v[162:163]
	v_mov_b32_e32 v184, v166
	v_mov_b32_e32 v185, v167
	v_mov_b32_e32 v222, 0x10000
	v_mov_b32_e32 v223, 0
	global_load_dwordx4 v[176:179], v[184:185], off
	global_load_dwordx4 v[180:183], v[184:185], off offset:256
	v_lshl_add_u64 v[184:185], v[222:223], 0, v[184:185]
	global_load_dwordx4 v[190:193], v[184:185], off
	global_load_dwordx4 v[194:197], v[184:185], off offset:256
	v_lshl_add_u64 v[184:185], v[222:223], 0, v[184:185]
	global_load_dwordx4 v[198:201], v[184:185], off
	global_load_dwordx4 v[202:205], v[184:185], off offset:256
	v_lshl_add_u64 v[184:185], v[222:223], 0, v[184:185]
	global_load_dwordx4 v[206:209], v[184:185], off
	global_load_dwordx4 v[210:213], v[184:185], off offset:256
	v_lshl_add_u64 v[184:185], v[222:223], 2, v[184:185]
	v_lshl_add_u64 v[184:185], v[222:223], 0, v[184:185]
	global_load_dwordx4 v[214:217], v[184:185], off
	global_load_dwordx4 v[218:221], v[184:185], off offset:256
	s_nop 0
	v_xor_b32_e32 v174, 32, v161
	s_waitcnt vmcnt(8)
	s_nop 1
	v_mov_b32_e32 v162, v176
	v_mov_b32_e32 v163, v177
	v_mov_b32_e32 v164, v178
	v_mov_b32_e32 v165, v179
	v_lshlrev_b32_e32 v168, 16, v162
	v_and_b32_e32 v169, 0xffff0000, v162
	v_lshlrev_b32_e32 v162, 16, v163
	v_and_b32_e32 v163, 0xffff0000, v163
	v_lshlrev_b32_e32 v170, 16, v164
	v_and_b32_e32 v171, 0xffff0000, v164
	v_lshlrev_b32_e32 v164, 16, v165
	v_and_b32_e32 v165, 0xffff0000, v165
	v_pk_add_f32 v[128:129], v[128:129], v[162:163]
	v_pk_add_f32 v[168:169], v[126:127], v[168:169]
	v_pk_add_f32 v[172:173], v[124:125], v[164:165]
	v_pk_add_f32 v[170:171], v[122:123], v[170:171]
	v_cvt_pk_bf16_f32 v124, v168, v169
	v_cvt_pk_bf16_f32 v125, v128, v129
	v_mul_f32_e32 v169, v169, v169
	v_cvt_pk_bf16_f32 v126, v170, v171
	v_cvt_pk_bf16_f32 v127, v172, v173
	s_nop 0
	v_mul_f32_e32 v129, v129, v129
	v_mul_f32_e32 v171, v171, v171
	v_mul_f32_e32 v173, v173, v173
	v_fmac_f32_e32 v169, v168, v168
	v_fmac_f32_e32 v129, v128, v128
	v_fmac_f32_e32 v171, v170, v170
	v_fmac_f32_e32 v173, v172, v172
	v_add_f32_e32 v128, v169, v129
	v_add_f32_e32 v129, v171, v173
	v_add_f32_e32 v170, v128, v129
	v_and_b32_e32 v123, 64, v161
	v_xor_b32_e32 v122, 16, v161
	v_add_u32_e32 v123, 64, v123
	v_cmp_lt_i32_e32 vcc, v122, v123
	global_store_dwordx4 v[166:167], v[124:127], off
	s_nop 1
	v_mov_b32_e32 v162, v180
	v_mov_b32_e32 v163, v181
	v_mov_b32_e32 v164, v182
	v_mov_b32_e32 v165, v183
	v_lshl_add_u64 v[184:185], v[222:223], 0, v[184:185]
	global_load_dwordx4 v[176:179], v[184:185], off
	global_load_dwordx4 v[180:183], v[184:185], off offset:256
	v_lshlrev_b32_e32 v128, 16, v162
	v_and_b32_e32 v129, 0xffff0000, v162
	v_lshlrev_b32_e32 v162, 16, v163
	v_and_b32_e32 v163, 0xffff0000, v163
	v_lshlrev_b32_e32 v168, 16, v164
	v_and_b32_e32 v169, 0xffff0000, v164
	v_lshlrev_b32_e32 v164, 16, v165
	v_and_b32_e32 v165, 0xffff0000, v165
	v_pk_add_f32 v[120:121], v[120:121], v[162:163]
	v_pk_add_f32 v[118:119], v[118:119], v[128:129]
	v_pk_add_f32 v[128:129], v[116:117], v[164:165]
	v_pk_add_f32 v[162:163], v[114:115], v[168:169]
	v_mul_f32_e32 v114, v119, v119
	v_mul_f32_e32 v115, v121, v121
	v_mul_f32_e32 v116, v163, v163
	v_mul_f32_e32 v117, v129, v129
	v_fmac_f32_e32 v114, v118, v118
	v_fmac_f32_e32 v115, v120, v120
	v_fmac_f32_e32 v116, v162, v162
	v_fmac_f32_e32 v117, v128, v128
	v_add_f32_e32 v114, v114, v115
	v_add_f32_e32 v115, v116, v117
	v_cndmask_b32_e32 v122, v161, v122, vcc
	v_add_f32_e32 v114, v114, v115
	v_lshlrev_b32_e32 v122, 2, v122
	v_add_f32_e32 v114, v170, v114
	ds_bpermute_b32 v115, v122, v114
	v_cmp_lt_i32_e32 vcc, v174, v123
	v_cvt_pk_bf16_f32 v118, v118, v119
	v_cvt_pk_bf16_f32 v119, v120, v121
	v_cvt_pk_bf16_f32 v120, v162, v163
	s_waitcnt lgkmcnt(0)
	v_add_f32_e32 v114, v114, v115
	v_cvt_pk_bf16_f32 v121, v128, v129
	v_cndmask_b32_e32 v116, v161, v174, vcc
	v_lshlrev_b32_e32 v116, 2, v116
	ds_bpermute_b32 v115, v116, v114
	global_store_dwordx4 v[166:167], v[118:121], off offset:256
	s_and_saveexec_b64 s[20:21], s[4:5]
	s_cbranch_execz .LBB0_561
	s_waitcnt lgkmcnt(0)
	v_add_f32_e32 v114, v114, v115
	v_fma_f32 v114, v114, s42, 0.5
	v_trunc_f32_e32 v114, v114
	v_mul_f32_e32 v115, 0x2f800000, v114
	v_floor_f32_e32 v115, v115
	v_fmac_f32_e32 v114, 0xcf800000, v115
	v_cvt_u32_f32_e32 v114, v114
	v_cvt_u32_f32_e32 v115, v115
	v_lshl_add_u64 v[118:119], v[150:151], 3, s[12:13]
	global_atomic_add_x2 v[118:119], v[114:115], off
.LBB0_561:
	s_or_b64 exec, exec, s[20:21]
	v_or_b32_e32 v114, 16, v150
	s_waitcnt lgkmcnt(0)
	v_ashrrev_i32_e32 v115, 31, v114
	v_lshlrev_b64 v[118:119], 12, v[114:115]
	v_lshl_add_u64 v[118:119], s[50:51], 0, v[118:119]
	v_lshl_add_u64 v[124:125], v[148:149], 1, v[118:119]
	s_nop 0
	s_waitcnt vmcnt(10)
	s_nop 1
	v_mov_b32_e32 v118, v190
	v_mov_b32_e32 v119, v191
	v_mov_b32_e32 v120, v192
	v_mov_b32_e32 v121, v193
	v_lshlrev_b32_e32 v126, 16, v118
	v_and_b32_e32 v127, 0xffff0000, v118
	v_lshlrev_b32_e32 v118, 16, v119
	v_and_b32_e32 v119, 0xffff0000, v119
	v_lshlrev_b32_e32 v128, 16, v120
	v_and_b32_e32 v129, 0xffff0000, v120
	v_lshlrev_b32_e32 v120, 16, v121
	v_and_b32_e32 v121, 0xffff0000, v121
	v_pk_add_f32 v[118:119], v[112:113], v[118:119]
	v_pk_add_f32 v[126:127], v[110:111], v[126:127]
	v_pk_add_f32 v[120:121], v[108:109], v[120:121]
	v_pk_add_f32 v[128:129], v[106:107], v[128:129]
	v_cvt_pk_bf16_f32 v106, v126, v127
	v_cvt_pk_bf16_f32 v107, v118, v119
	v_mul_f32_e32 v117, v127, v127
	v_cvt_pk_bf16_f32 v108, v128, v129
	v_cvt_pk_bf16_f32 v109, v120, v121
	s_nop 0
	v_mul_f32_e32 v119, v119, v119
	v_mul_f32_e32 v123, v129, v129
	v_mul_f32_e32 v121, v121, v121
	v_fmac_f32_e32 v117, v126, v126
	v_fmac_f32_e32 v119, v118, v118
	v_fmac_f32_e32 v123, v128, v128
	v_fmac_f32_e32 v121, v120, v120
	v_add_f32_e32 v117, v117, v119
	v_add_f32_e32 v118, v123, v121
	v_add_f32_e32 v117, v117, v118
	global_store_dwordx4 v[124:125], v[106:109], off
	s_nop 1
	v_mov_b32_e32 v110, v194
	v_mov_b32_e32 v111, v195
	v_mov_b32_e32 v112, v196
	v_mov_b32_e32 v113, v197
	v_lshl_add_u64 v[184:185], v[222:223], 0, v[184:185]
	global_load_dwordx4 v[190:193], v[184:185], off
	global_load_dwordx4 v[194:197], v[184:185], off offset:256
	v_lshlrev_b32_e32 v118, 16, v110
	v_and_b32_e32 v119, 0xffff0000, v110
	v_lshlrev_b32_e32 v110, 16, v111
	v_and_b32_e32 v111, 0xffff0000, v111
	v_lshlrev_b32_e32 v120, 16, v112
	v_and_b32_e32 v121, 0xffff0000, v112
	v_lshlrev_b32_e32 v112, 16, v113
	v_and_b32_e32 v113, 0xffff0000, v113
	v_pk_add_f32 v[104:105], v[104:105], v[110:111]
	v_pk_add_f32 v[102:103], v[102:103], v[118:119]
	v_pk_add_f32 v[110:111], v[100:101], v[112:113]
	v_pk_add_f32 v[112:113], v[98:99], v[120:121]
	v_mul_f32_e32 v98, v103, v103
	v_mul_f32_e32 v99, v105, v105
	v_mul_f32_e32 v100, v113, v113
	v_mul_f32_e32 v101, v111, v111
	v_fmac_f32_e32 v98, v102, v102
	v_fmac_f32_e32 v99, v104, v104
	v_fmac_f32_e32 v100, v112, v112
	v_fmac_f32_e32 v101, v110, v110
	v_add_f32_e32 v98, v98, v99
	v_add_f32_e32 v99, v100, v101
	v_add_f32_e32 v98, v98, v99
	v_add_f32_e32 v98, v117, v98
	ds_bpermute_b32 v99, v122, v98
	v_cvt_pk_bf16_f32 v100, v102, v103
	v_cvt_pk_bf16_f32 v101, v104, v105
	v_cvt_pk_bf16_f32 v102, v112, v113
	v_cvt_pk_bf16_f32 v103, v110, v111
	s_waitcnt lgkmcnt(0)
	v_add_f32_e32 v98, v98, v99
	ds_bpermute_b32 v99, v116, v98
	global_store_dwordx4 v[124:125], v[100:103], off offset:256
	s_and_saveexec_b64 s[20:21], s[4:5]
	s_cbranch_execz .LBB0_563
	s_waitcnt lgkmcnt(0)
	v_add_f32_e32 v98, v98, v99
	v_fma_f32 v98, v98, s42, 0.5
	v_trunc_f32_e32 v98, v98
	v_mul_f32_e32 v99, 0x2f800000, v98
	v_floor_f32_e32 v99, v99
	v_fmac_f32_e32 v98, 0xcf800000, v99
	v_cvt_u32_f32_e32 v98, v98
	v_cvt_u32_f32_e32 v99, v99
	v_lshl_add_u64 v[100:101], v[114:115], 3, s[12:13]
	global_atomic_add_x2 v[100:101], v[98:99], off
.LBB0_563:
	s_or_b64 exec, exec, s[20:21]
	v_or_b32_e32 v98, 32, v150
	s_waitcnt lgkmcnt(0)
	v_ashrrev_i32_e32 v99, 31, v98
	v_lshlrev_b64 v[100:101], 12, v[98:99]
	v_lshl_add_u64 v[100:101], s[50:51], 0, v[100:101]
	v_lshl_add_u64 v[104:105], v[148:149], 1, v[100:101]
	s_nop 0
	s_waitcnt vmcnt(12)
	s_nop 1
	v_mov_b32_e32 v100, v198
	v_mov_b32_e32 v101, v199
	v_mov_b32_e32 v102, v200
	v_mov_b32_e32 v103, v201
	v_lshlrev_b32_e32 v106, 16, v100
	v_and_b32_e32 v107, 0xffff0000, v100
	v_lshlrev_b32_e32 v100, 16, v101
	v_and_b32_e32 v101, 0xffff0000, v101
	v_lshlrev_b32_e32 v108, 16, v102
	v_and_b32_e32 v109, 0xffff0000, v102
	v_lshlrev_b32_e32 v102, 16, v103
	v_and_b32_e32 v103, 0xffff0000, v103
	v_pk_add_f32 v[100:101], v[96:97], v[100:101]
	v_pk_add_f32 v[106:107], v[94:95], v[106:107]
	v_pk_add_f32 v[102:103], v[92:93], v[102:103]
	v_pk_add_f32 v[108:109], v[90:91], v[108:109]
	v_cvt_pk_bf16_f32 v90, v106, v107
	v_cvt_pk_bf16_f32 v91, v100, v101
	v_mul_f32_e32 v107, v107, v107
	v_cvt_pk_bf16_f32 v92, v108, v109
	v_cvt_pk_bf16_f32 v93, v102, v103
	s_nop 0
	v_mul_f32_e32 v101, v101, v101
	v_mul_f32_e32 v109, v109, v109
	v_mul_f32_e32 v103, v103, v103
	v_fmac_f32_e32 v107, v106, v106
	v_fmac_f32_e32 v101, v100, v100
	v_fmac_f32_e32 v109, v108, v108
	v_fmac_f32_e32 v103, v102, v102
	v_add_f32_e32 v100, v107, v101
	v_add_f32_e32 v101, v109, v103
	v_add_f32_e32 v106, v100, v101
	global_store_dwordx4 v[104:105], v[90:93], off
	s_nop 1
	v_mov_b32_e32 v94, v202
	v_mov_b32_e32 v95, v203
	v_mov_b32_e32 v96, v204
	v_mov_b32_e32 v97, v205
	v_lshl_add_u64 v[184:185], v[222:223], 0, v[184:185]
	global_load_dwordx4 v[198:201], v[184:185], off
	global_load_dwordx4 v[202:205], v[184:185], off offset:256
	v_lshlrev_b32_e32 v100, 16, v94
	v_and_b32_e32 v101, 0xffff0000, v94
	v_lshlrev_b32_e32 v94, 16, v95
	v_and_b32_e32 v95, 0xffff0000, v95
	v_lshlrev_b32_e32 v102, 16, v96
	v_and_b32_e32 v103, 0xffff0000, v96
	v_lshlrev_b32_e32 v96, 16, v97
	v_and_b32_e32 v97, 0xffff0000, v97
	v_pk_add_f32 v[88:89], v[88:89], v[94:95]
	v_pk_add_f32 v[86:87], v[86:87], v[100:101]
	v_pk_add_f32 v[94:95], v[84:85], v[96:97]
	v_pk_add_f32 v[96:97], v[82:83], v[102:103]
	v_mul_f32_e32 v82, v87, v87
	v_mul_f32_e32 v83, v89, v89
	v_mul_f32_e32 v84, v97, v97
	v_mul_f32_e32 v85, v95, v95
	v_fmac_f32_e32 v82, v86, v86
	v_fmac_f32_e32 v83, v88, v88
	v_fmac_f32_e32 v84, v96, v96
	v_fmac_f32_e32 v85, v94, v94
	v_add_f32_e32 v82, v82, v83
	v_add_f32_e32 v83, v84, v85
	v_add_f32_e32 v82, v82, v83
	v_add_f32_e32 v82, v106, v82
	ds_bpermute_b32 v83, v122, v82
	v_cvt_pk_bf16_f32 v84, v86, v87
	v_cvt_pk_bf16_f32 v85, v88, v89
	v_cvt_pk_bf16_f32 v86, v96, v97
	v_cvt_pk_bf16_f32 v87, v94, v95
	s_waitcnt lgkmcnt(0)
	v_add_f32_e32 v82, v82, v83
	ds_bpermute_b32 v83, v116, v82
	global_store_dwordx4 v[104:105], v[84:87], off offset:256
	s_and_saveexec_b64 s[20:21], s[4:5]
	s_cbranch_execz .LBB0_565
	s_waitcnt lgkmcnt(0)
	v_add_f32_e32 v82, v82, v83
	v_fma_f32 v82, v82, s42, 0.5
	v_trunc_f32_e32 v82, v82
	v_mul_f32_e32 v83, 0x2f800000, v82
	v_floor_f32_e32 v83, v83
	v_fmac_f32_e32 v82, 0xcf800000, v83
	v_cvt_u32_f32_e32 v82, v82
	v_cvt_u32_f32_e32 v83, v83
	v_lshl_add_u64 v[84:85], v[98:99], 3, s[12:13]
	global_atomic_add_x2 v[84:85], v[82:83], off
.LBB0_565:
	s_or_b64 exec, exec, s[20:21]
	v_or_b32_e32 v82, 48, v150
	s_waitcnt lgkmcnt(0)
	v_ashrrev_i32_e32 v83, 31, v82
	v_lshlrev_b64 v[84:85], 12, v[82:83]
	v_lshl_add_u64 v[84:85], s[50:51], 0, v[84:85]
	v_lshl_add_u64 v[88:89], v[148:149], 1, v[84:85]
	s_nop 0
	s_waitcnt vmcnt(14)
	s_nop 1
	v_mov_b32_e32 v84, v206
	v_mov_b32_e32 v85, v207
	v_mov_b32_e32 v86, v208
	v_mov_b32_e32 v87, v209
	v_lshlrev_b32_e32 v90, 16, v84
	v_and_b32_e32 v91, 0xffff0000, v84
	v_lshlrev_b32_e32 v84, 16, v85
	v_and_b32_e32 v85, 0xffff0000, v85
	v_lshlrev_b32_e32 v92, 16, v86
	v_and_b32_e32 v93, 0xffff0000, v86
	v_lshlrev_b32_e32 v86, 16, v87
	v_and_b32_e32 v87, 0xffff0000, v87
	v_pk_add_f32 v[84:85], v[80:81], v[84:85]
	v_pk_add_f32 v[90:91], v[78:79], v[90:91]
	v_pk_add_f32 v[86:87], v[76:77], v[86:87]
	v_pk_add_f32 v[92:93], v[74:75], v[92:93]
	v_cvt_pk_bf16_f32 v74, v90, v91
	v_cvt_pk_bf16_f32 v75, v84, v85
	v_mul_f32_e32 v91, v91, v91
	v_cvt_pk_bf16_f32 v76, v92, v93
	v_cvt_pk_bf16_f32 v77, v86, v87
	s_nop 0
	v_mul_f32_e32 v85, v85, v85
	v_mul_f32_e32 v93, v93, v93
	v_mul_f32_e32 v87, v87, v87
	v_fmac_f32_e32 v91, v90, v90
	v_fmac_f32_e32 v85, v84, v84
	v_fmac_f32_e32 v93, v92, v92
	v_fmac_f32_e32 v87, v86, v86
	v_add_f32_e32 v84, v91, v85
	v_add_f32_e32 v85, v93, v87
	v_add_f32_e32 v90, v84, v85
	global_store_dwordx4 v[88:89], v[74:77], off
	s_nop 1
	v_mov_b32_e32 v78, v210
	v_mov_b32_e32 v79, v211
	v_mov_b32_e32 v80, v212
	v_mov_b32_e32 v81, v213
	v_lshlrev_b32_e32 v84, 16, v78
	v_and_b32_e32 v85, 0xffff0000, v78
	v_lshlrev_b32_e32 v78, 16, v79
	v_and_b32_e32 v79, 0xffff0000, v79
	v_lshlrev_b32_e32 v86, 16, v80
	v_and_b32_e32 v87, 0xffff0000, v80
	v_lshlrev_b32_e32 v80, 16, v81
	v_and_b32_e32 v81, 0xffff0000, v81
	v_pk_add_f32 v[72:73], v[72:73], v[78:79]
	v_pk_add_f32 v[70:71], v[70:71], v[84:85]
	v_pk_add_f32 v[78:79], v[68:69], v[80:81]
	v_pk_add_f32 v[80:81], v[66:67], v[86:87]
	v_mul_f32_e32 v66, v71, v71
	v_mul_f32_e32 v67, v73, v73
	v_mul_f32_e32 v68, v81, v81
	v_mul_f32_e32 v69, v79, v79
	v_fmac_f32_e32 v66, v70, v70
	v_fmac_f32_e32 v67, v72, v72
	v_fmac_f32_e32 v68, v80, v80
	v_fmac_f32_e32 v69, v78, v78
	v_add_f32_e32 v66, v66, v67
	v_add_f32_e32 v67, v68, v69
	v_add_f32_e32 v66, v66, v67
	v_add_f32_e32 v66, v90, v66
	ds_bpermute_b32 v67, v122, v66
	v_cvt_pk_bf16_f32 v68, v70, v71
	v_cvt_pk_bf16_f32 v69, v72, v73
	v_cvt_pk_bf16_f32 v70, v80, v81
	v_cvt_pk_bf16_f32 v71, v78, v79
	s_waitcnt lgkmcnt(0)
	v_add_f32_e32 v66, v66, v67
	ds_bpermute_b32 v67, v116, v66
	global_store_dwordx4 v[88:89], v[68:71], off offset:256
	s_and_saveexec_b64 s[20:21], s[4:5]
	s_cbranch_execz .LBB0_567
	s_waitcnt lgkmcnt(0)
	v_add_f32_e32 v66, v66, v67
	v_fma_f32 v66, v66, s42, 0.5
	v_trunc_f32_e32 v66, v66
	v_mul_f32_e32 v67, 0x2f800000, v66
	v_floor_f32_e32 v67, v67
	v_fmac_f32_e32 v66, 0xcf800000, v67
	v_cvt_u32_f32_e32 v66, v66
	v_cvt_u32_f32_e32 v67, v67
	v_lshl_add_u64 v[68:69], v[82:83], 3, s[12:13]
	global_atomic_add_x2 v[68:69], v[66:67], off
.LBB0_567:
	s_or_b64 exec, exec, s[20:21]
	v_add_u32_e32 v66, 0x80, v150
	s_waitcnt lgkmcnt(0)
	v_ashrrev_i32_e32 v67, 31, v66
	v_lshlrev_b64 v[68:69], 12, v[66:67]
	v_lshl_add_u64 v[68:69], s[50:51], 0, v[68:69]
	v_lshl_add_u64 v[72:73], v[148:149], 1, v[68:69]
	s_nop 0
	s_waitcnt vmcnt(14)
	s_nop 1
	v_mov_b32_e32 v68, v214
	v_mov_b32_e32 v69, v215
	v_mov_b32_e32 v70, v216
	v_mov_b32_e32 v71, v217
	v_lshlrev_b32_e32 v74, 16, v68
	v_and_b32_e32 v75, 0xffff0000, v68
	v_lshlrev_b32_e32 v68, 16, v69
	v_and_b32_e32 v69, 0xffff0000, v69
	v_lshlrev_b32_e32 v76, 16, v70
	v_and_b32_e32 v77, 0xffff0000, v70
	v_lshlrev_b32_e32 v70, 16, v71
	v_and_b32_e32 v71, 0xffff0000, v71
	v_pk_add_f32 v[68:69], v[64:65], v[68:69]
	v_pk_add_f32 v[74:75], v[62:63], v[74:75]
	v_pk_add_f32 v[70:71], v[60:61], v[70:71]
	v_pk_add_f32 v[76:77], v[58:59], v[76:77]
	v_cvt_pk_bf16_f32 v58, v74, v75
	v_cvt_pk_bf16_f32 v59, v68, v69
	v_mul_f32_e32 v75, v75, v75
	v_cvt_pk_bf16_f32 v60, v76, v77
	v_cvt_pk_bf16_f32 v61, v70, v71
	s_nop 0
	v_mul_f32_e32 v69, v69, v69
	v_mul_f32_e32 v77, v77, v77
	v_mul_f32_e32 v71, v71, v71
	v_fmac_f32_e32 v75, v74, v74
	v_fmac_f32_e32 v69, v68, v68
	v_fmac_f32_e32 v77, v76, v76
	v_fmac_f32_e32 v71, v70, v70
	v_add_f32_e32 v68, v75, v69
	v_add_f32_e32 v69, v77, v71
	v_add_f32_e32 v74, v68, v69
	global_store_dwordx4 v[72:73], v[58:61], off
	s_nop 1
	v_mov_b32_e32 v62, v218
	v_mov_b32_e32 v63, v219
	v_mov_b32_e32 v64, v220
	v_mov_b32_e32 v65, v221
	v_lshlrev_b32_e32 v68, 16, v62
	v_and_b32_e32 v69, 0xffff0000, v62
	v_lshlrev_b32_e32 v62, 16, v63
	v_and_b32_e32 v63, 0xffff0000, v63
	v_lshlrev_b32_e32 v70, 16, v64
	v_and_b32_e32 v71, 0xffff0000, v64
	v_lshlrev_b32_e32 v64, 16, v65
	v_and_b32_e32 v65, 0xffff0000, v65
	v_pk_add_f32 v[56:57], v[56:57], v[62:63]
	v_pk_add_f32 v[54:55], v[54:55], v[68:69]
	v_pk_add_f32 v[62:63], v[52:53], v[64:65]
	v_pk_add_f32 v[64:65], v[50:51], v[70:71]
	v_mul_f32_e32 v50, v55, v55
	v_mul_f32_e32 v51, v57, v57
	v_mul_f32_e32 v52, v65, v65
	v_mul_f32_e32 v53, v63, v63
	v_fmac_f32_e32 v50, v54, v54
	v_fmac_f32_e32 v51, v56, v56
	v_fmac_f32_e32 v52, v64, v64
	v_fmac_f32_e32 v53, v62, v62
	v_add_f32_e32 v50, v50, v51
	v_add_f32_e32 v51, v52, v53
	v_add_f32_e32 v50, v50, v51
	v_add_f32_e32 v50, v74, v50
	ds_bpermute_b32 v51, v122, v50
	v_cvt_pk_bf16_f32 v52, v54, v55
	v_cvt_pk_bf16_f32 v53, v56, v57
	v_cvt_pk_bf16_f32 v54, v64, v65
	v_cvt_pk_bf16_f32 v55, v62, v63
	s_waitcnt lgkmcnt(0)
	v_add_f32_e32 v50, v50, v51
	ds_bpermute_b32 v51, v116, v50
	global_store_dwordx4 v[72:73], v[52:55], off offset:256
	s_and_saveexec_b64 s[20:21], s[4:5]
	s_cbranch_execz .LBB0_569
	s_waitcnt lgkmcnt(0)
	v_add_f32_e32 v50, v50, v51
	v_fma_f32 v50, v50, s42, 0.5
	v_trunc_f32_e32 v50, v50
	v_mul_f32_e32 v51, 0x2f800000, v50
	v_floor_f32_e32 v51, v51
	v_fmac_f32_e32 v50, 0xcf800000, v51
	v_cvt_u32_f32_e32 v50, v50
	v_cvt_u32_f32_e32 v51, v51
	v_lshl_add_u64 v[52:53], v[66:67], 3, s[12:13]
	global_atomic_add_x2 v[52:53], v[50:51], off
.LBB0_569:
	s_or_b64 exec, exec, s[20:21]
	v_add_u32_e32 v50, 0x90, v150
	s_waitcnt lgkmcnt(0)
	v_ashrrev_i32_e32 v51, 31, v50
	v_lshlrev_b64 v[52:53], 12, v[50:51]
	v_lshl_add_u64 v[52:53], s[50:51], 0, v[52:53]
	v_lshl_add_u64 v[56:57], v[148:149], 1, v[52:53]
	s_nop 0
	s_waitcnt vmcnt(13)
	s_nop 1
	v_mov_b32_e32 v52, v176
	v_mov_b32_e32 v53, v177
	v_mov_b32_e32 v54, v178
	v_mov_b32_e32 v55, v179
	v_lshlrev_b32_e32 v58, 16, v52
	v_and_b32_e32 v59, 0xffff0000, v52
	v_lshlrev_b32_e32 v52, 16, v53
	v_and_b32_e32 v53, 0xffff0000, v53
	v_lshlrev_b32_e32 v60, 16, v54
	v_and_b32_e32 v61, 0xffff0000, v54
	v_lshlrev_b32_e32 v54, 16, v55
	v_and_b32_e32 v55, 0xffff0000, v55
	v_pk_add_f32 v[52:53], v[48:49], v[52:53]
	v_pk_add_f32 v[58:59], v[46:47], v[58:59]
	v_pk_add_f32 v[54:55], v[44:45], v[54:55]
	v_pk_add_f32 v[60:61], v[42:43], v[60:61]
	v_cvt_pk_bf16_f32 v42, v58, v59
	v_cvt_pk_bf16_f32 v43, v52, v53
	v_mul_f32_e32 v59, v59, v59
	v_cvt_pk_bf16_f32 v44, v60, v61
	v_cvt_pk_bf16_f32 v45, v54, v55
	s_nop 0
	v_mul_f32_e32 v53, v53, v53
	v_mul_f32_e32 v61, v61, v61
	v_mul_f32_e32 v55, v55, v55
	v_fmac_f32_e32 v59, v58, v58
	v_fmac_f32_e32 v53, v52, v52
	v_fmac_f32_e32 v61, v60, v60
	v_fmac_f32_e32 v55, v54, v54
	v_add_f32_e32 v52, v59, v53
	v_add_f32_e32 v53, v61, v55
	v_add_f32_e32 v58, v52, v53
	global_store_dwordx4 v[56:57], v[42:45], off
	s_nop 1
	v_mov_b32_e32 v46, v180
	v_mov_b32_e32 v47, v181
	v_mov_b32_e32 v48, v182
	v_mov_b32_e32 v49, v183
	v_lshlrev_b32_e32 v52, 16, v46
	v_and_b32_e32 v53, 0xffff0000, v46
	v_lshlrev_b32_e32 v46, 16, v47
	v_and_b32_e32 v47, 0xffff0000, v47
	v_lshlrev_b32_e32 v54, 16, v48
	v_and_b32_e32 v55, 0xffff0000, v48
	v_lshlrev_b32_e32 v48, 16, v49
	v_and_b32_e32 v49, 0xffff0000, v49
	v_pk_add_f32 v[40:41], v[40:41], v[46:47]
	v_pk_add_f32 v[38:39], v[38:39], v[52:53]
	v_pk_add_f32 v[46:47], v[36:37], v[48:49]
	v_pk_add_f32 v[48:49], v[34:35], v[54:55]
	v_mul_f32_e32 v34, v39, v39
	v_mul_f32_e32 v35, v41, v41
	v_mul_f32_e32 v36, v49, v49
	v_mul_f32_e32 v37, v47, v47
	v_fmac_f32_e32 v34, v38, v38
	v_fmac_f32_e32 v35, v40, v40
	v_fmac_f32_e32 v36, v48, v48
	v_fmac_f32_e32 v37, v46, v46
	v_add_f32_e32 v34, v34, v35
	v_add_f32_e32 v35, v36, v37
	v_add_f32_e32 v34, v34, v35
	v_add_f32_e32 v34, v58, v34
	ds_bpermute_b32 v35, v122, v34
	v_cvt_pk_bf16_f32 v36, v38, v39
	v_cvt_pk_bf16_f32 v37, v40, v41
	v_cvt_pk_bf16_f32 v38, v48, v49
	v_cvt_pk_bf16_f32 v39, v46, v47
	s_waitcnt lgkmcnt(0)
	v_add_f32_e32 v34, v34, v35
	ds_bpermute_b32 v35, v116, v34
	global_store_dwordx4 v[56:57], v[36:39], off offset:256
	s_and_saveexec_b64 s[20:21], s[4:5]
	s_cbranch_execz .LBB0_571
	s_waitcnt lgkmcnt(0)
	v_add_f32_e32 v34, v34, v35
	v_fma_f32 v34, v34, s42, 0.5
	v_trunc_f32_e32 v34, v34
	v_mul_f32_e32 v35, 0x2f800000, v34
	v_floor_f32_e32 v35, v35
	v_fmac_f32_e32 v34, 0xcf800000, v35
	v_cvt_u32_f32_e32 v34, v34
	v_cvt_u32_f32_e32 v35, v35
	v_lshl_add_u64 v[36:37], v[50:51], 3, s[12:13]
	global_atomic_add_x2 v[36:37], v[34:35], off
.LBB0_571:
	s_or_b64 exec, exec, s[20:21]
	v_add_u32_e32 v34, 0xa0, v150
	s_waitcnt lgkmcnt(0)
	v_ashrrev_i32_e32 v35, 31, v34
	v_lshlrev_b64 v[36:37], 12, v[34:35]
	v_lshl_add_u64 v[36:37], s[50:51], 0, v[36:37]
	v_lshl_add_u64 v[40:41], v[148:149], 1, v[36:37]
	s_nop 0
	s_waitcnt vmcnt(11)
	s_nop 1
	v_mov_b32_e32 v36, v190
	v_mov_b32_e32 v37, v191
	v_mov_b32_e32 v38, v192
	v_mov_b32_e32 v39, v193
	v_lshlrev_b32_e32 v42, 16, v36
	v_and_b32_e32 v43, 0xffff0000, v36
	v_lshlrev_b32_e32 v36, 16, v37
	v_and_b32_e32 v37, 0xffff0000, v37
	v_lshlrev_b32_e32 v44, 16, v38
	v_and_b32_e32 v45, 0xffff0000, v38
	v_lshlrev_b32_e32 v38, 16, v39
	v_and_b32_e32 v39, 0xffff0000, v39
	v_pk_add_f32 v[36:37], v[32:33], v[36:37]
	v_pk_add_f32 v[42:43], v[30:31], v[42:43]
	v_pk_add_f32 v[38:39], v[28:29], v[38:39]
	v_pk_add_f32 v[44:45], v[26:27], v[44:45]
	v_cvt_pk_bf16_f32 v26, v42, v43
	v_cvt_pk_bf16_f32 v27, v36, v37
	v_mul_f32_e32 v43, v43, v43
	v_cvt_pk_bf16_f32 v28, v44, v45
	v_cvt_pk_bf16_f32 v29, v38, v39
	s_nop 0
	v_mul_f32_e32 v37, v37, v37
	v_mul_f32_e32 v45, v45, v45
	v_mul_f32_e32 v39, v39, v39
	v_fmac_f32_e32 v43, v42, v42
	v_fmac_f32_e32 v37, v36, v36
	v_fmac_f32_e32 v45, v44, v44
	v_fmac_f32_e32 v39, v38, v38
	v_add_f32_e32 v36, v43, v37
	v_add_f32_e32 v37, v45, v39
	v_add_f32_e32 v42, v36, v37
	global_store_dwordx4 v[40:41], v[26:29], off
	s_nop 1
	v_mov_b32_e32 v30, v194
	v_mov_b32_e32 v31, v195
	v_mov_b32_e32 v32, v196
	v_mov_b32_e32 v33, v197
	v_lshlrev_b32_e32 v36, 16, v30
	v_and_b32_e32 v37, 0xffff0000, v30
	v_lshlrev_b32_e32 v30, 16, v31
	v_and_b32_e32 v31, 0xffff0000, v31
	v_lshlrev_b32_e32 v38, 16, v32
	v_and_b32_e32 v39, 0xffff0000, v32
	v_lshlrev_b32_e32 v32, 16, v33
	v_and_b32_e32 v33, 0xffff0000, v33
	v_pk_add_f32 v[24:25], v[24:25], v[30:31]
	v_pk_add_f32 v[22:23], v[22:23], v[36:37]
	v_pk_add_f32 v[30:31], v[20:21], v[32:33]
	v_pk_add_f32 v[32:33], v[18:19], v[38:39]
	v_mul_f32_e32 v18, v23, v23
	v_mul_f32_e32 v19, v25, v25
	v_mul_f32_e32 v20, v33, v33
	v_mul_f32_e32 v21, v31, v31
	v_fmac_f32_e32 v18, v22, v22
	v_fmac_f32_e32 v19, v24, v24
	v_fmac_f32_e32 v20, v32, v32
	v_fmac_f32_e32 v21, v30, v30
	v_add_f32_e32 v18, v18, v19
	v_add_f32_e32 v19, v20, v21
	v_add_f32_e32 v18, v18, v19
	v_add_f32_e32 v18, v42, v18
	ds_bpermute_b32 v19, v122, v18
	v_cvt_pk_bf16_f32 v20, v22, v23
	v_cvt_pk_bf16_f32 v21, v24, v25
	v_cvt_pk_bf16_f32 v22, v32, v33
	v_cvt_pk_bf16_f32 v23, v30, v31
	s_waitcnt lgkmcnt(0)
	v_add_f32_e32 v18, v18, v19
	ds_bpermute_b32 v19, v116, v18
	global_store_dwordx4 v[40:41], v[20:23], off offset:256
	s_and_saveexec_b64 s[20:21], s[4:5]
	s_cbranch_execz .LBB0_573
	s_waitcnt lgkmcnt(0)
	v_add_f32_e32 v18, v18, v19
	v_fma_f32 v18, v18, s42, 0.5
	v_trunc_f32_e32 v18, v18
	v_mul_f32_e32 v19, 0x2f800000, v18
	v_floor_f32_e32 v19, v19
	v_fmac_f32_e32 v18, 0xcf800000, v19
	v_cvt_u32_f32_e32 v18, v18
	v_cvt_u32_f32_e32 v19, v19
	v_lshl_add_u64 v[20:21], v[34:35], 3, s[12:13]
	global_atomic_add_x2 v[20:21], v[18:19], off
.LBB0_573:
	s_or_b64 exec, exec, s[20:21]
	v_add_u32_e32 v18, 0xb0, v150
	s_waitcnt lgkmcnt(0)
	v_ashrrev_i32_e32 v19, 31, v18
	v_lshlrev_b64 v[20:21], 12, v[18:19]
	v_lshl_add_u64 v[20:21], s[50:51], 0, v[20:21]
	v_lshl_add_u64 v[24:25], v[148:149], 1, v[20:21]
	s_nop 0
	s_waitcnt vmcnt(9)
	s_nop 1
	v_mov_b32_e32 v20, v198
	v_mov_b32_e32 v21, v199
	v_mov_b32_e32 v22, v200
	v_mov_b32_e32 v23, v201
	v_lshlrev_b32_e32 v26, 16, v20
	v_and_b32_e32 v27, 0xffff0000, v20
	v_lshlrev_b32_e32 v20, 16, v21
	v_and_b32_e32 v21, 0xffff0000, v21
	v_lshlrev_b32_e32 v28, 16, v22
	v_and_b32_e32 v29, 0xffff0000, v22
	v_lshlrev_b32_e32 v22, 16, v23
	v_and_b32_e32 v23, 0xffff0000, v23
	v_pk_add_f32 v[20:21], v[16:17], v[20:21]
	v_pk_add_f32 v[26:27], v[14:15], v[26:27]
	v_pk_add_f32 v[22:23], v[12:13], v[22:23]
	v_pk_add_f32 v[28:29], v[10:11], v[28:29]
	v_cvt_pk_bf16_f32 v10, v26, v27
	v_cvt_pk_bf16_f32 v11, v20, v21
	v_mul_f32_e32 v27, v27, v27
	v_cvt_pk_bf16_f32 v12, v28, v29
	v_cvt_pk_bf16_f32 v13, v22, v23
	s_nop 0
	v_mul_f32_e32 v21, v21, v21
	v_mul_f32_e32 v29, v29, v29
	v_mul_f32_e32 v23, v23, v23
	v_fmac_f32_e32 v27, v26, v26
	v_fmac_f32_e32 v21, v20, v20
	v_fmac_f32_e32 v29, v28, v28
	v_fmac_f32_e32 v23, v22, v22
	v_add_f32_e32 v20, v27, v21
	v_add_f32_e32 v21, v29, v23
	v_add_f32_e32 v26, v20, v21
	global_store_dwordx4 v[24:25], v[10:13], off
	s_nop 1
	v_mov_b32_e32 v14, v202
	v_mov_b32_e32 v15, v203
	v_mov_b32_e32 v16, v204
	v_mov_b32_e32 v17, v205
	v_lshlrev_b32_e32 v20, 16, v14
	v_and_b32_e32 v21, 0xffff0000, v14
	v_lshlrev_b32_e32 v14, 16, v15
	v_and_b32_e32 v15, 0xffff0000, v15
	v_lshlrev_b32_e32 v22, 16, v16
	v_and_b32_e32 v23, 0xffff0000, v16
	v_lshlrev_b32_e32 v16, 16, v17
	v_and_b32_e32 v17, 0xffff0000, v17
	v_pk_add_f32 v[8:9], v[8:9], v[14:15]
	v_pk_add_f32 v[6:7], v[6:7], v[20:21]
	v_pk_add_f32 v[14:15], v[4:5], v[16:17]
	v_pk_add_f32 v[16:17], v[2:3], v[22:23]
	v_mul_f32_e32 v2, v7, v7
	v_mul_f32_e32 v3, v9, v9
	v_mul_f32_e32 v4, v17, v17
	v_mul_f32_e32 v5, v15, v15
	v_fmac_f32_e32 v2, v6, v6
	v_fmac_f32_e32 v3, v8, v8
	v_fmac_f32_e32 v4, v16, v16
	v_fmac_f32_e32 v5, v14, v14
	v_add_f32_e32 v2, v2, v3
	v_add_f32_e32 v3, v4, v5
	v_add_f32_e32 v2, v2, v3
	v_add_f32_e32 v2, v26, v2
	ds_bpermute_b32 v3, v122, v2
	v_cvt_pk_bf16_f32 v4, v6, v7
	v_cvt_pk_bf16_f32 v5, v8, v9
	v_cvt_pk_bf16_f32 v6, v16, v17
	v_cvt_pk_bf16_f32 v7, v14, v15
	s_waitcnt lgkmcnt(0)
	v_add_f32_e32 v2, v2, v3
	ds_bpermute_b32 v3, v116, v2
	global_store_dwordx4 v[24:25], v[4:7], off offset:256
	s_and_saveexec_b64 s[20:21], s[4:5]
	s_cbranch_execz .LBB0_575
	s_waitcnt lgkmcnt(0)
	v_add_f32_e32 v2, v2, v3
	v_fma_f32 v2, v2, s42, 0.5
	v_trunc_f32_e32 v2, v2
	v_mul_f32_e32 v3, 0x2f800000, v2
	v_floor_f32_e32 v3, v3
	v_fmac_f32_e32 v2, 0xcf800000, v3
	v_cvt_u32_f32_e32 v2, v2
	v_cvt_u32_f32_e32 v3, v3
	v_lshl_add_u64 v[4:5], v[18:19], 3, s[12:13]
	global_atomic_add_x2 v[4:5], v[2:3], off

.LBB0_851:
	v_lshl_add_u32 v152, s30, 8, v154
	v_lshl_or_b32 v150, s57, 8, v156
	v_ashrrev_i32_e32 v153, 31, v152
	v_ashrrev_i32_e32 v151, 31, v150
	v_lshlrev_b64 v[148:149], 11, v[152:153]
	v_lshl_add_u64 v[148:149], v[148:149], 0, v[150:151]
	v_lshl_add_u64 v[166:167], v[148:149], 1, s[50:51]
	v_mov_b32_e32 v222, v166
	v_mov_b32_e32 v223, v167
	v_mov_b32_e32 v240, 0x10000
	v_mov_b32_e32 v241, 0
	global_load_dwordx4 v[174:177], v[222:223], off
	global_load_dwordx4 v[178:181], v[222:223], off offset:256
	v_lshl_add_u64 v[222:223], v[240:241], 0, v[222:223]
	global_load_dwordx4 v[182:185], v[222:223], off
	global_load_dwordx4 v[186:189], v[222:223], off offset:256
	v_lshl_add_u64 v[222:223], v[240:241], 0, v[222:223]
	global_load_dwordx4 v[190:193], v[222:223], off
	global_load_dwordx4 v[194:197], v[222:223], off offset:256
	v_lshl_add_u64 v[222:223], v[240:241], 0, v[222:223]
	global_load_dwordx4 v[198:201], v[222:223], off
	global_load_dwordx4 v[202:205], v[222:223], off offset:256
	v_lshl_add_u64 v[222:223], v[240:241], 2, v[222:223]
	v_lshl_add_u64 v[222:223], v[240:241], 0, v[222:223]
	global_load_dwordx4 v[206:209], v[222:223], off
	global_load_dwordx4 v[210:213], v[222:223], off offset:256
	v_lshl_add_u64 v[222:223], v[240:241], 0, v[222:223]
	global_load_dwordx4 v[214:217], v[222:223], off
	global_load_dwordx4 v[218:221], v[222:223], off offset:256
	s_nop 0
	v_lshl_add_u64 v[168:169], v[148:149], 2, s[28:29]
	s_andn2_b64 vcc, exec, s[4:5]
	s_mov_b64 s[4:5], -1
	s_waitcnt vmcnt(10)
	s_nop 1
	v_mov_b32_e32 v162, v174
	v_mov_b32_e32 v163, v175
	v_mov_b32_e32 v164, v176
	v_mov_b32_e32 v165, v177
	v_lshlrev_b32_e32 v170, 16, v162
	v_and_b32_e32 v171, 0xffff0000, v162
	v_lshlrev_b32_e32 v162, 16, v163
	v_and_b32_e32 v163, 0xffff0000, v163
	v_lshlrev_b32_e32 v172, 16, v164
	v_and_b32_e32 v173, 0xffff0000, v164
	v_lshlrev_b32_e32 v164, 16, v165
	v_and_b32_e32 v165, 0xffff0000, v165
	v_pk_add_f32 v[128:129], v[128:129], v[162:163]
	v_pk_add_f32 v[126:127], v[126:127], v[170:171]
	v_pk_add_f32 v[124:125], v[124:125], v[164:165]
	v_pk_add_f32 v[122:123], v[122:123], v[172:173]
	global_store_dwordx4 v[168:169], v[126:129], off
	global_store_dwordx4 v[168:169], v[122:125], off offset:16
	s_nop 0
	v_or_b32_e32 v126, 16, v152
	v_ashrrev_i32_e32 v127, 31, v126
	v_lshlrev_b64 v[126:127], 11, v[126:127]
	v_lshl_add_u64 v[126:127], v[126:127], 0, v[150:151]
	v_lshl_add_u64 v[128:129], v[126:127], 1, s[50:51]
	s_nop 1
	v_mov_b32_e32 v122, v178
	v_mov_b32_e32 v123, v179
	v_mov_b32_e32 v124, v180
	v_mov_b32_e32 v125, v181
	v_lshl_add_u64 v[222:223], v[240:241], 0, v[222:223]
	global_load_dwordx4 v[174:177], v[222:223], off
	global_load_dwordx4 v[178:181], v[222:223], off offset:256
	v_lshlrev_b32_e32 v162, 16, v122
	v_and_b32_e32 v163, 0xffff0000, v122
	v_lshlrev_b32_e32 v122, 16, v123
	v_and_b32_e32 v123, 0xffff0000, v123
	v_lshlrev_b32_e32 v164, 16, v124
	v_and_b32_e32 v165, 0xffff0000, v124
	v_lshlrev_b32_e32 v124, 16, v125
	v_and_b32_e32 v125, 0xffff0000, v125
	v_pk_add_f32 v[120:121], v[120:121], v[122:123]
	v_pk_add_f32 v[118:119], v[118:119], v[162:163]
	v_pk_add_f32 v[116:117], v[116:117], v[124:125]
	v_pk_add_f32 v[114:115], v[114:115], v[164:165]
	global_store_dwordx4 v[168:169], v[118:121], off offset:512
	global_store_dwordx4 v[168:169], v[114:117], off offset:528
	s_nop 0
	v_lshl_add_u64 v[118:119], v[126:127], 2, s[28:29]
	s_waitcnt vmcnt(14)
	s_nop 1
	v_mov_b32_e32 v114, v182
	v_mov_b32_e32 v115, v183
	v_mov_b32_e32 v116, v184
	v_mov_b32_e32 v117, v185
	v_lshlrev_b32_e32 v120, 16, v114
	v_and_b32_e32 v121, 0xffff0000, v114
	v_lshlrev_b32_e32 v114, 16, v115
	v_and_b32_e32 v115, 0xffff0000, v115
	v_lshlrev_b32_e32 v122, 16, v116
	v_and_b32_e32 v123, 0xffff0000, v116
	v_lshlrev_b32_e32 v116, 16, v117
	v_and_b32_e32 v117, 0xffff0000, v117
	v_pk_add_f32 v[112:113], v[112:113], v[114:115]
	v_pk_add_f32 v[110:111], v[110:111], v[120:121]
	v_pk_add_f32 v[108:109], v[108:109], v[116:117]
	v_pk_add_f32 v[106:107], v[106:107], v[122:123]
	global_store_dwordx4 v[118:119], v[110:113], off
	global_store_dwordx4 v[118:119], v[106:109], off offset:16
	s_nop 0
	v_or_b32_e32 v110, 32, v152
	v_ashrrev_i32_e32 v111, 31, v110
	v_lshlrev_b64 v[110:111], 11, v[110:111]
	v_lshl_add_u64 v[110:111], v[110:111], 0, v[150:151]
	v_lshl_add_u64 v[112:113], v[110:111], 1, s[50:51]
	s_nop 1
	v_mov_b32_e32 v106, v186
	v_mov_b32_e32 v107, v187
	v_mov_b32_e32 v108, v188
	v_mov_b32_e32 v109, v189
	v_lshl_add_u64 v[222:223], v[240:241], 0, v[222:223]
	global_load_dwordx4 v[182:185], v[222:223], off
	global_load_dwordx4 v[186:189], v[222:223], off offset:256
	v_lshlrev_b32_e32 v114, 16, v106
	v_and_b32_e32 v115, 0xffff0000, v106
	v_lshlrev_b32_e32 v106, 16, v107
	v_and_b32_e32 v107, 0xffff0000, v107
	v_lshlrev_b32_e32 v116, 16, v108
	v_and_b32_e32 v117, 0xffff0000, v108
	v_lshlrev_b32_e32 v108, 16, v109
	v_and_b32_e32 v109, 0xffff0000, v109
	v_pk_add_f32 v[104:105], v[104:105], v[106:107]
	v_pk_add_f32 v[102:103], v[102:103], v[114:115]
	v_pk_add_f32 v[100:101], v[100:101], v[108:109]
	v_pk_add_f32 v[98:99], v[98:99], v[116:117]
	global_store_dwordx4 v[118:119], v[102:105], off offset:512
	global_store_dwordx4 v[118:119], v[98:101], off offset:528
	s_nop 0
	v_lshl_add_u64 v[102:103], v[110:111], 2, s[28:29]
	s_waitcnt vmcnt(18)
	s_nop 1
	v_mov_b32_e32 v98, v190
	v_mov_b32_e32 v99, v191
	v_mov_b32_e32 v100, v192
	v_mov_b32_e32 v101, v193
	v_lshlrev_b32_e32 v104, 16, v98
	v_and_b32_e32 v105, 0xffff0000, v98
	v_lshlrev_b32_e32 v98, 16, v99
	v_and_b32_e32 v99, 0xffff0000, v99
	v_lshlrev_b32_e32 v106, 16, v100
	v_and_b32_e32 v107, 0xffff0000, v100
	v_lshlrev_b32_e32 v100, 16, v101
	v_and_b32_e32 v101, 0xffff0000, v101
	v_pk_add_f32 v[96:97], v[96:97], v[98:99]
	v_pk_add_f32 v[94:95], v[94:95], v[104:105]
	v_pk_add_f32 v[92:93], v[92:93], v[100:101]
	v_pk_add_f32 v[90:91], v[90:91], v[106:107]
	global_store_dwordx4 v[102:103], v[94:97], off
	global_store_dwordx4 v[102:103], v[90:93], off offset:16
	s_nop 0
	v_or_b32_e32 v94, 48, v152
	v_ashrrev_i32_e32 v95, 31, v94
	v_lshlrev_b64 v[94:95], 11, v[94:95]
	v_lshl_add_u64 v[94:95], v[94:95], 0, v[150:151]
	v_lshl_add_u64 v[96:97], v[94:95], 1, s[50:51]
	s_nop 1
	v_mov_b32_e32 v90, v194
	v_mov_b32_e32 v91, v195
	v_mov_b32_e32 v92, v196
	v_mov_b32_e32 v93, v197
	v_lshlrev_b32_e32 v98, 16, v90
	v_and_b32_e32 v99, 0xffff0000, v90
	v_lshlrev_b32_e32 v90, 16, v91
	v_and_b32_e32 v91, 0xffff0000, v91
	v_lshlrev_b32_e32 v100, 16, v92
	v_and_b32_e32 v101, 0xffff0000, v92
	v_lshlrev_b32_e32 v92, 16, v93
	v_and_b32_e32 v93, 0xffff0000, v93
	v_pk_add_f32 v[88:89], v[88:89], v[90:91]
	v_pk_add_f32 v[86:87], v[86:87], v[98:99]
	v_pk_add_f32 v[84:85], v[84:85], v[92:93]
	v_pk_add_f32 v[82:83], v[82:83], v[100:101]
	global_store_dwordx4 v[102:103], v[86:89], off offset:512
	global_store_dwordx4 v[102:103], v[82:85], off offset:528
	s_nop 0
	v_lshl_add_u64 v[86:87], v[94:95], 2, s[28:29]
	s_waitcnt vmcnt(20)
	s_nop 1
	v_mov_b32_e32 v82, v198
	v_mov_b32_e32 v83, v199
	v_mov_b32_e32 v84, v200
	v_mov_b32_e32 v85, v201
	v_lshlrev_b32_e32 v88, 16, v82
	v_and_b32_e32 v89, 0xffff0000, v82
	v_lshlrev_b32_e32 v82, 16, v83
	v_and_b32_e32 v83, 0xffff0000, v83
	v_lshlrev_b32_e32 v90, 16, v84
	v_and_b32_e32 v91, 0xffff0000, v84
	v_lshlrev_b32_e32 v84, 16, v85
	v_and_b32_e32 v85, 0xffff0000, v85
	v_pk_add_f32 v[80:81], v[80:81], v[82:83]
	v_pk_add_f32 v[78:79], v[78:79], v[88:89]
	v_pk_add_f32 v[76:77], v[76:77], v[84:85]
	v_pk_add_f32 v[74:75], v[74:75], v[90:91]
	global_store_dwordx4 v[86:87], v[78:81], off
	global_store_dwordx4 v[86:87], v[74:77], off offset:16
	s_nop 0
	v_lshl_add_u64 v[78:79], v[148:149], 0, s[12:13]
	v_lshl_add_u64 v[80:81], v[78:79], 1, s[50:51]
	s_nop 1
	v_mov_b32_e32 v74, v202
	v_mov_b32_e32 v75, v203
	v_mov_b32_e32 v76, v204
	v_mov_b32_e32 v77, v205
	v_lshlrev_b32_e32 v82, 16, v74
	v_and_b32_e32 v83, 0xffff0000, v74
	v_lshlrev_b32_e32 v74, 16, v75
	v_and_b32_e32 v75, 0xffff0000, v75
	v_lshlrev_b32_e32 v84, 16, v76
	v_and_b32_e32 v85, 0xffff0000, v76
	v_lshlrev_b32_e32 v76, 16, v77
	v_and_b32_e32 v77, 0xffff0000, v77
	v_pk_add_f32 v[72:73], v[72:73], v[74:75]
	v_pk_add_f32 v[70:71], v[70:71], v[82:83]
	v_pk_add_f32 v[68:69], v[68:69], v[76:77]
	v_pk_add_f32 v[66:67], v[66:67], v[84:85]
	global_store_dwordx4 v[86:87], v[70:73], off offset:512
	global_store_dwordx4 v[86:87], v[66:69], off offset:528
	s_nop 0
	v_lshl_add_u64 v[70:71], v[78:79], 2, s[28:29]
	s_waitcnt vmcnt(22)
	s_nop 1
	v_mov_b32_e32 v66, v206
	v_mov_b32_e32 v67, v207
	v_mov_b32_e32 v68, v208
	v_mov_b32_e32 v69, v209
	v_lshlrev_b32_e32 v72, 16, v66
	v_and_b32_e32 v73, 0xffff0000, v66
	v_lshlrev_b32_e32 v66, 16, v67
	v_and_b32_e32 v67, 0xffff0000, v67
	v_lshlrev_b32_e32 v74, 16, v68
	v_and_b32_e32 v75, 0xffff0000, v68
	v_lshlrev_b32_e32 v68, 16, v69
	v_and_b32_e32 v69, 0xffff0000, v69
	v_pk_add_f32 v[64:65], v[64:65], v[66:67]
	v_pk_add_f32 v[62:63], v[62:63], v[72:73]
	v_pk_add_f32 v[60:61], v[60:61], v[68:69]
	v_pk_add_f32 v[58:59], v[58:59], v[74:75]
	global_store_dwordx4 v[70:71], v[62:65], off
	global_store_dwordx4 v[70:71], v[58:61], off offset:16
	s_nop 0
	v_lshl_add_u64 v[62:63], v[148:149], 0, s[14:15]
	v_lshl_add_u64 v[64:65], v[62:63], 1, s[50:51]
	s_nop 1
	v_mov_b32_e32 v58, v210
	v_mov_b32_e32 v59, v211
	v_mov_b32_e32 v60, v212
	v_mov_b32_e32 v61, v213
	v_lshlrev_b32_e32 v66, 16, v58
	v_and_b32_e32 v67, 0xffff0000, v58
	v_lshlrev_b32_e32 v58, 16, v59
	v_and_b32_e32 v59, 0xffff0000, v59
	v_lshlrev_b32_e32 v68, 16, v60
	v_and_b32_e32 v69, 0xffff0000, v60
	v_lshlrev_b32_e32 v60, 16, v61
	v_and_b32_e32 v61, 0xffff0000, v61
	v_pk_add_f32 v[56:57], v[56:57], v[58:59]
	v_pk_add_f32 v[54:55], v[54:55], v[66:67]
	v_pk_add_f32 v[52:53], v[52:53], v[60:61]
	v_pk_add_f32 v[50:51], v[50:51], v[68:69]
	global_store_dwordx4 v[70:71], v[54:57], off offset:512
	global_store_dwordx4 v[70:71], v[50:53], off offset:528
	s_nop 0
	v_lshl_add_u64 v[54:55], v[62:63], 2, s[28:29]
	s_waitcnt vmcnt(24)
	s_nop 1
	v_mov_b32_e32 v50, v214
	v_mov_b32_e32 v51, v215
	v_mov_b32_e32 v52, v216
	v_mov_b32_e32 v53, v217
	v_lshlrev_b32_e32 v56, 16, v50
	v_and_b32_e32 v57, 0xffff0000, v50
	v_lshlrev_b32_e32 v50, 16, v51
	v_and_b32_e32 v51, 0xffff0000, v51
	v_lshlrev_b32_e32 v58, 16, v52
	v_and_b32_e32 v59, 0xffff0000, v52
	v_lshlrev_b32_e32 v52, 16, v53
	v_and_b32_e32 v53, 0xffff0000, v53
	v_pk_add_f32 v[48:49], v[48:49], v[50:51]
	v_pk_add_f32 v[46:47], v[46:47], v[56:57]
	v_pk_add_f32 v[44:45], v[44:45], v[52:53]
	v_pk_add_f32 v[42:43], v[42:43], v[58:59]
	global_store_dwordx4 v[54:55], v[46:49], off
	global_store_dwordx4 v[54:55], v[42:45], off offset:16
	s_nop 0
	v_lshl_add_u64 v[46:47], v[148:149], 0, s[16:17]
	v_lshl_add_u64 v[48:49], v[46:47], 1, s[50:51]
	s_nop 1
	v_mov_b32_e32 v42, v218
	v_mov_b32_e32 v43, v219
	v_mov_b32_e32 v44, v220
	v_mov_b32_e32 v45, v221
	v_lshlrev_b32_e32 v50, 16, v42
	v_and_b32_e32 v51, 0xffff0000, v42
	v_lshlrev_b32_e32 v42, 16, v43
	v_and_b32_e32 v43, 0xffff0000, v43
	v_lshlrev_b32_e32 v52, 16, v44
	v_and_b32_e32 v53, 0xffff0000, v44
	v_lshlrev_b32_e32 v44, 16, v45
	v_and_b32_e32 v45, 0xffff0000, v45
	v_pk_add_f32 v[40:41], v[40:41], v[42:43]
	v_pk_add_f32 v[38:39], v[38:39], v[50:51]
	v_pk_add_f32 v[36:37], v[36:37], v[44:45]
	v_pk_add_f32 v[34:35], v[34:35], v[52:53]
	global_store_dwordx4 v[54:55], v[38:41], off offset:512
	global_store_dwordx4 v[54:55], v[34:37], off offset:528
	s_nop 0
	v_lshl_add_u64 v[38:39], v[46:47], 2, s[28:29]
	s_waitcnt vmcnt(24)
	s_nop 1
	v_mov_b32_e32 v34, v174
	v_mov_b32_e32 v35, v175
	v_mov_b32_e32 v36, v176
	v_mov_b32_e32 v37, v177
	v_lshlrev_b32_e32 v40, 16, v34
	v_and_b32_e32 v41, 0xffff0000, v34
	v_lshlrev_b32_e32 v34, 16, v35
	v_and_b32_e32 v35, 0xffff0000, v35
	v_lshlrev_b32_e32 v42, 16, v36
	v_and_b32_e32 v43, 0xffff0000, v36
	v_lshlrev_b32_e32 v36, 16, v37
	v_and_b32_e32 v37, 0xffff0000, v37
	v_pk_add_f32 v[32:33], v[32:33], v[34:35]
	v_pk_add_f32 v[30:31], v[30:31], v[40:41]
	v_pk_add_f32 v[28:29], v[28:29], v[36:37]
	v_pk_add_f32 v[26:27], v[26:27], v[42:43]
	global_store_dwordx4 v[38:39], v[30:33], off
	global_store_dwordx4 v[38:39], v[26:29], off offset:16
	s_nop 0
	v_lshl_add_u64 v[30:31], v[148:149], 0, s[18:19]
	v_lshl_add_u64 v[32:33], v[30:31], 1, s[50:51]
	s_nop 1
	v_mov_b32_e32 v26, v178
	v_mov_b32_e32 v27, v179
	v_mov_b32_e32 v28, v180
	v_mov_b32_e32 v29, v181
	v_lshlrev_b32_e32 v34, 16, v26
	v_and_b32_e32 v35, 0xffff0000, v26
	v_lshlrev_b32_e32 v26, 16, v27
	v_and_b32_e32 v27, 0xffff0000, v27
	v_lshlrev_b32_e32 v36, 16, v28
	v_and_b32_e32 v37, 0xffff0000, v28
	v_lshlrev_b32_e32 v28, 16, v29
	v_and_b32_e32 v29, 0xffff0000, v29
	v_pk_add_f32 v[24:25], v[24:25], v[26:27]
	v_pk_add_f32 v[22:23], v[22:23], v[34:35]
	v_pk_add_f32 v[20:21], v[20:21], v[28:29]
	v_pk_add_f32 v[18:19], v[18:19], v[36:37]
	global_store_dwordx4 v[38:39], v[22:25], off offset:512
	global_store_dwordx4 v[38:39], v[18:21], off offset:528
	s_nop 0
	v_lshl_add_u64 v[22:23], v[30:31], 2, s[28:29]
	s_waitcnt vmcnt(22)
	s_nop 1
	v_mov_b32_e32 v18, v182
	v_mov_b32_e32 v19, v183
	v_mov_b32_e32 v20, v184
	v_mov_b32_e32 v21, v185
	v_lshlrev_b32_e32 v24, 16, v18
	v_and_b32_e32 v25, 0xffff0000, v18
	v_lshlrev_b32_e32 v18, 16, v19
	v_and_b32_e32 v19, 0xffff0000, v19
	v_lshlrev_b32_e32 v26, 16, v20
	v_and_b32_e32 v27, 0xffff0000, v20
	v_lshlrev_b32_e32 v20, 16, v21
	v_and_b32_e32 v21, 0xffff0000, v21
	v_pk_add_f32 v[16:17], v[16:17], v[18:19]
	v_pk_add_f32 v[14:15], v[14:15], v[24:25]
	v_pk_add_f32 v[12:13], v[12:13], v[20:21]
	v_pk_add_f32 v[10:11], v[10:11], v[26:27]
	global_store_dwordx4 v[22:23], v[14:17], off
	global_store_dwordx4 v[22:23], v[10:13], off offset:16
	s_nop 0
	s_nop 1
	v_mov_b32_e32 v10, v186
	v_mov_b32_e32 v11, v187
	v_mov_b32_e32 v12, v188
	v_mov_b32_e32 v13, v189
	v_lshlrev_b32_e32 v14, 16, v10
	v_and_b32_e32 v15, 0xffff0000, v10
	v_lshlrev_b32_e32 v10, 16, v11
	v_and_b32_e32 v11, 0xffff0000, v11
	v_lshlrev_b32_e32 v16, 16, v12
	v_and_b32_e32 v17, 0xffff0000, v12
	v_lshlrev_b32_e32 v12, 16, v13
	v_and_b32_e32 v13, 0xffff0000, v13
	v_pk_add_f32 v[8:9], v[8:9], v[10:11]
	v_pk_add_f32 v[6:7], v[6:7], v[14:15]
	v_pk_add_f32 v[4:5], v[4:5], v[12:13]
	v_pk_add_f32 v[2:3], v[2:3], v[16:17]
	global_store_dwordx4 v[22:23], v[6:9], off offset:512
	global_store_dwordx4 v[22:23], v[2:5], off offset:528
	s_cbranch_vccnz .LBB0_840
	s_andn2_b64 vcc, exec, s[6:7]
	s_cbranch_vccnz .LBB0_839
	s_barrier
	s_branch .LBB0_839
